# GEMM K-loops: M0 write moved ahead of the DMA address add so the add provides the M0->LDS-DMA wait state; 56 s_nop 0 dropped (on top of v62)
# baseline (speedup 1.0000x reference)
.Lpeel_in:
	s_mov_b64 s[26:27], 0
	v_mov_b64_e32 v[178:179], v[174:175]
	v_mov_b64_e32 v[180:181], v[168:169]
	v_mov_b32_e32 v186, v176
	v_mov_b32_e32 v172, v170
	ds_read_b128 v[0:3], v193
	ds_read_b128 v[8:11], v193 offset:2048
	ds_read_b128 v[4:7], v195
	ds_read_b128 v[12:15], v195 offset:2048
	s_add_u32 s15, s24, 0x80
	s_addc_u32 s23, s25, 0
	s_and_b64 s[26:27], s[26:27], exec
	s_cselect_b32 s29, s19, s23
	s_cselect_b32 s28, s18, s15
	s_cselect_b32 s27, s17, s3
	s_cselect_b32 s26, s16, s2
	v_lshl_add_u64 v[16:17], s[24:25], 0, v[168:169]
	s_add_i32 m0, s47, 0xc000
	ds_read_b128 v[218:221], v192
	ds_read_b128 v[226:229], v192 offset:2048
	ds_read_b128 v[222:225], v194
	ds_read_b128 v[230:233], v194 offset:2048
	ds_read_b128 v[234:237], v192 offset:4096
	ds_read_b128 v[242:245], v192 offset:6144
	ds_read_b128 v[238:241], v194 offset:4096
	ds_read_b128 v[246:249], v194 offset:6144
	global_load_lds_dwordx4 v[16:17], off
	s_add_i32 m0, s47, 0xe000
	v_lshl_add_u64 v[16:17], s[24:25], 0, v[174:175]
	global_load_lds_dwordx4 v[16:17], off
	s_waitcnt lgkmcnt(8)
	s_barrier
	s_waitcnt lgkmcnt(0)
	s_setprio 1
	v_mfma_scale_f32_16x16x128_f8f6f4 v[156:159], v[0:7], v[218:225], 0, v191, v191 op_sel_hi:[0,0,0]
	v_mfma_scale_f32_16x16x128_f8f6f4 v[152:155], v[8:15], v[218:225], 0, v191, v191 op_sel_hi:[0,0,0]
	v_mfma_scale_f32_16x16x128_f8f6f4 v[148:151], v[0:7], v[226:233], 0, v191, v191 op_sel_hi:[0,0,0]
	v_mfma_scale_f32_16x16x128_f8f6f4 v[144:147], v[8:15], v[226:233], 0, v191, v191 op_sel_hi:[0,0,0]
	v_mfma_scale_f32_16x16x128_f8f6f4 v[140:143], v[0:7], v[234:241], 0, v191, v191 op_sel_hi:[0,0,0]
	v_mfma_scale_f32_16x16x128_f8f6f4 v[136:139], v[8:15], v[234:241], 0, v191, v191 op_sel_hi:[0,0,0]
	v_mfma_scale_f32_16x16x128_f8f6f4 v[132:135], v[0:7], v[242:249], 0, v191, v191 op_sel_hi:[0,0,0]
	v_mfma_scale_f32_16x16x128_f8f6f4 v[128:131], v[8:15], v[242:249], 0, v191, v191 op_sel_hi:[0,0,0]
	s_setprio 0
	s_barrier
	s_mov_b32 m0, s30
	v_lshl_add_u64 v[182:183], s[26:27], 0, v[162:163]
	ds_read_b128 v[16:19], v193 offset:16384
	ds_read_b128 v[24:27], v193 offset:18432
	ds_read_b128 v[20:23], v195 offset:16384
	ds_read_b128 v[28:31], v195 offset:18432
	global_load_lds_dwordx4 v[182:183], off
	s_mov_b32 m0, s46
	v_lshl_add_u64 v[184:185], s[26:27], 0, v[164:165]
	global_load_lds_dwordx4 v[184:185], off
	s_barrier
	s_waitcnt lgkmcnt(0)
	s_setprio 1
	v_mfma_scale_f32_16x16x128_f8f6f4 v[92:95], v[16:23], v[218:225], 0, v191, v191 op_sel_hi:[0,0,0]
	v_mfma_scale_f32_16x16x128_f8f6f4 v[88:91], v[24:31], v[218:225], 0, v191, v191 op_sel_hi:[0,0,0]
	v_mfma_scale_f32_16x16x128_f8f6f4 v[84:87], v[16:23], v[226:233], 0, v191, v191 op_sel_hi:[0,0,0]
	v_mfma_scale_f32_16x16x128_f8f6f4 v[80:83], v[24:31], v[226:233], 0, v191, v191 op_sel_hi:[0,0,0]
	v_mfma_scale_f32_16x16x128_f8f6f4 v[76:79], v[16:23], v[234:241], 0, v191, v191 op_sel_hi:[0,0,0]
	v_mfma_scale_f32_16x16x128_f8f6f4 v[72:75], v[24:31], v[234:241], 0, v191, v191 op_sel_hi:[0,0,0]
	v_mfma_scale_f32_16x16x128_f8f6f4 v[68:71], v[16:23], v[242:249], 0, v191, v191 op_sel_hi:[0,0,0]
	v_mfma_scale_f32_16x16x128_f8f6f4 v[64:67], v[24:31], v[242:249], 0, v191, v191 op_sel_hi:[0,0,0]
	s_setprio 0
	s_mov_b32 m0, s47
	s_barrier
	ds_read_b128 v[218:221], v192 offset:16384
	ds_read_b128 v[226:229], v192 offset:18432
	ds_read_b128 v[222:225], v194 offset:16384
	ds_read_b128 v[230:233], v194 offset:18432
	ds_read_b128 v[234:237], v192 offset:20480
	ds_read_b128 v[242:245], v192 offset:22528
	ds_read_b128 v[238:241], v194 offset:20480
	ds_read_b128 v[246:249], v194 offset:22528
	global_load_lds_dwordx4 v172, s[28:29]
	s_mov_b32 m0, s83
	v_mov_b32_e32 v187, v173
	global_load_lds_dwordx4 v186, s[28:29]
	s_barrier
	s_waitcnt lgkmcnt(0)
	v_lshl_add_u64 v[188:189], s[28:29], 0, v[172:173]
	v_lshl_add_u64 v[186:187], s[28:29], 0, v[186:187]
	s_setprio 1
	s_waitcnt lgkmcnt(0)
	v_mfma_scale_f32_16x16x128_f8f6f4 v[124:127], v[0:7], v[218:225], 0, v191, v191 op_sel_hi:[0,0,0]
	v_mfma_scale_f32_16x16x128_f8f6f4 v[120:123], v[8:15], v[218:225], 0, v191, v191 op_sel_hi:[0,0,0]
	v_mfma_scale_f32_16x16x128_f8f6f4 v[116:119], v[0:7], v[226:233], 0, v191, v191 op_sel_hi:[0,0,0]
	v_mfma_scale_f32_16x16x128_f8f6f4 v[112:115], v[8:15], v[226:233], 0, v191, v191 op_sel_hi:[0,0,0]
	v_mfma_scale_f32_16x16x128_f8f6f4 v[108:111], v[0:7], v[234:241], 0, v191, v191 op_sel_hi:[0,0,0]
	v_mfma_scale_f32_16x16x128_f8f6f4 v[104:107], v[8:15], v[234:241], 0, v191, v191 op_sel_hi:[0,0,0]
	v_mfma_scale_f32_16x16x128_f8f6f4 v[100:103], v[0:7], v[242:249], 0, v191, v191 op_sel_hi:[0,0,0]
	v_mfma_scale_f32_16x16x128_f8f6f4 v[96:99], v[8:15], v[242:249], 0, v191, v191 op_sel_hi:[0,0,0]
	s_setprio 0
	s_barrier
	s_add_u32 s72, s26, 0x20000
	s_addc_u32 s73, s27, 0
	s_mov_b32 m0, s82
	v_lshl_add_u64 v[0:1], s[72:73], 0, v[162:163]
	global_load_lds_dwordx4 v[0:1], off
	s_mov_b32 m0, s80
	v_lshl_add_u64 v[0:1], s[72:73], 0, v[164:165]
	global_load_lds_dwordx4 v[0:1], off
	s_waitcnt vmcnt(6)
	s_barrier
	s_setprio 1
	v_mfma_scale_f32_16x16x128_f8f6f4 v[60:63], v[16:23], v[218:225], 0, v191, v191 op_sel_hi:[0,0,0]
	v_mfma_scale_f32_16x16x128_f8f6f4 v[56:59], v[24:31], v[218:225], 0, v191, v191 op_sel_hi:[0,0,0]
	v_mfma_scale_f32_16x16x128_f8f6f4 v[52:55], v[16:23], v[226:233], 0, v191, v191 op_sel_hi:[0,0,0]
	v_mfma_scale_f32_16x16x128_f8f6f4 v[48:51], v[24:31], v[226:233], 0, v191, v191 op_sel_hi:[0,0,0]
	v_mfma_scale_f32_16x16x128_f8f6f4 v[44:47], v[16:23], v[234:241], 0, v191, v191 op_sel_hi:[0,0,0]
	v_mfma_scale_f32_16x16x128_f8f6f4 v[40:43], v[24:31], v[234:241], 0, v191, v191 op_sel_hi:[0,0,0]
	v_mfma_scale_f32_16x16x128_f8f6f4 v[36:39], v[16:23], v[242:249], 0, v191, v191 op_sel_hi:[0,0,0]
	v_mfma_scale_f32_16x16x128_f8f6f4 v[32:35], v[24:31], v[242:249], 0, v191, v191 op_sel_hi:[0,0,0]
	s_setprio 0
	s_barrier
	ds_read_b128 v[0:3], v193 offset:32768
	ds_read_b128 v[8:11], v193 offset:34816
	ds_read_b128 v[4:7], v195 offset:32768
	ds_read_b128 v[12:15], v195 offset:34816
	s_mov_b32 m0, s81
	v_lshl_add_u64 v[180:181], s[28:29], 0, v[180:181]
	ds_read_b128 v[16:19], v192 offset:32768
	ds_read_b128 v[24:27], v192 offset:34816
	ds_read_b128 v[20:23], v194 offset:32768
	ds_read_b128 v[28:31], v194 offset:34816
	ds_read_b128 v[218:221], v192 offset:36864
	ds_read_b128 v[226:229], v192 offset:38912
	ds_read_b128 v[222:225], v194 offset:36864
	ds_read_b128 v[230:233], v194 offset:38912
	global_load_lds_dwordx4 v[180:181], off
	s_mov_b32 m0, s50
	v_lshl_add_u64 v[178:179], s[28:29], 0, v[178:179]
	global_load_lds_dwordx4 v[178:179], off
	s_waitcnt lgkmcnt(8)
	s_barrier
	s_waitcnt lgkmcnt(0)
	s_setprio 1
	v_mfma_scale_f32_16x16x128_f8f6f4 v[156:159], v[0:7], v[16:23], v[156:159], v191, v191 op_sel_hi:[0,0,0]
	v_mfma_scale_f32_16x16x128_f8f6f4 v[152:155], v[8:15], v[16:23], v[152:155], v191, v191 op_sel_hi:[0,0,0]
	v_mfma_scale_f32_16x16x128_f8f6f4 v[148:151], v[0:7], v[24:31], v[148:151], v191, v191 op_sel_hi:[0,0,0]
	v_mfma_scale_f32_16x16x128_f8f6f4 v[144:147], v[8:15], v[24:31], v[144:147], v191, v191 op_sel_hi:[0,0,0]
	v_mfma_scale_f32_16x16x128_f8f6f4 v[140:143], v[0:7], v[218:225], v[140:143], v191, v191 op_sel_hi:[0,0,0]
	v_mfma_scale_f32_16x16x128_f8f6f4 v[136:139], v[8:15], v[218:225], v[136:139], v191, v191 op_sel_hi:[0,0,0]
	v_mfma_scale_f32_16x16x128_f8f6f4 v[132:135], v[0:7], v[226:233], v[132:135], v191, v191 op_sel_hi:[0,0,0]
	v_mfma_scale_f32_16x16x128_f8f6f4 v[128:131], v[8:15], v[226:233], v[128:131], v191, v191 op_sel_hi:[0,0,0]
	s_setprio 0
	s_barrier
	s_mov_b32 m0, s51
	v_lshl_add_u64 v[178:179], v[182:183], 0, s[40:41]
	ds_read_b128 v[234:237], v193 offset:49152
	ds_read_b128 v[242:245], v193 offset:51200
	ds_read_b128 v[238:241], v195 offset:49152
	ds_read_b128 v[246:249], v195 offset:51200
	global_load_lds_dwordx4 v[178:179], off
	s_mov_b32 m0, s70
	v_lshl_add_u64 v[178:179], v[184:185], 0, s[40:41]
	global_load_lds_dwordx4 v[178:179], off
	s_barrier
	s_waitcnt lgkmcnt(0)
	s_setprio 1
	v_mfma_scale_f32_16x16x128_f8f6f4 v[92:95], v[234:241], v[16:23], v[92:95], v191, v191 op_sel_hi:[0,0,0]
	v_mfma_scale_f32_16x16x128_f8f6f4 v[88:91], v[242:249], v[16:23], v[88:91], v191, v191 op_sel_hi:[0,0,0]
	v_mfma_scale_f32_16x16x128_f8f6f4 v[84:87], v[234:241], v[24:31], v[84:87], v191, v191 op_sel_hi:[0,0,0]
	v_mfma_scale_f32_16x16x128_f8f6f4 v[80:83], v[242:249], v[24:31], v[80:83], v191, v191 op_sel_hi:[0,0,0]
	v_mfma_scale_f32_16x16x128_f8f6f4 v[76:79], v[234:241], v[218:225], v[76:79], v191, v191 op_sel_hi:[0,0,0]
	v_mfma_scale_f32_16x16x128_f8f6f4 v[72:75], v[242:249], v[218:225], v[72:75], v191, v191 op_sel_hi:[0,0,0]
	v_mfma_scale_f32_16x16x128_f8f6f4 v[68:71], v[234:241], v[226:233], v[68:71], v191, v191 op_sel_hi:[0,0,0]
	v_mfma_scale_f32_16x16x128_f8f6f4 v[64:67], v[242:249], v[226:233], v[64:67], v191, v191 op_sel_hi:[0,0,0]
	s_setprio 0
	s_mov_b32 m0, s71
	v_lshl_add_u64 v[188:189], v[188:189], 0, s[40:41]
	s_barrier
	ds_read_b128 v[16:19], v192 offset:49152
	ds_read_b128 v[24:27], v192 offset:51200
	ds_read_b128 v[20:23], v194 offset:49152
	ds_read_b128 v[28:31], v194 offset:51200
	ds_read_b128 v[178:181], v192 offset:53248
	ds_read_b128 v[218:221], v192 offset:55296
	ds_read_b128 v[182:185], v194 offset:53248
	ds_read_b128 v[222:225], v194 offset:55296
	global_load_lds_dwordx4 v[188:189], off
	s_mov_b32 m0, s87
	v_lshl_add_u64 v[186:187], v[186:187], 0, s[40:41]
	global_load_lds_dwordx4 v[186:187], off
	s_barrier
	s_waitcnt lgkmcnt(0)
	s_setprio 1
	v_mfma_scale_f32_16x16x128_f8f6f4 v[124:127], v[0:7], v[16:23], v[124:127], v191, v191 op_sel_hi:[0,0,0]
	v_mfma_scale_f32_16x16x128_f8f6f4 v[120:123], v[8:15], v[16:23], v[120:123], v191, v191 op_sel_hi:[0,0,0]
	v_mfma_scale_f32_16x16x128_f8f6f4 v[116:119], v[0:7], v[24:31], v[116:119], v191, v191 op_sel_hi:[0,0,0]
	v_mfma_scale_f32_16x16x128_f8f6f4 v[112:115], v[8:15], v[24:31], v[112:115], v191, v191 op_sel_hi:[0,0,0]
	v_mfma_scale_f32_16x16x128_f8f6f4 v[108:111], v[0:7], v[178:185], v[108:111], v191, v191 op_sel_hi:[0,0,0]
	v_mfma_scale_f32_16x16x128_f8f6f4 v[104:107], v[8:15], v[178:185], v[104:107], v191, v191 op_sel_hi:[0,0,0]
	v_mfma_scale_f32_16x16x128_f8f6f4 v[100:103], v[0:7], v[218:225], v[100:103], v191, v191 op_sel_hi:[0,0,0]
	v_mfma_scale_f32_16x16x128_f8f6f4 v[96:99], v[8:15], v[218:225], v[96:99], v191, v191 op_sel_hi:[0,0,0]
	s_setprio 0
	s_barrier
	s_add_u32 s26, s26, 0x20080
	s_addc_u32 s27, s27, 0
	s_mov_b32 m0, s1
	v_lshl_add_u64 v[0:1], s[26:27], 0, v[162:163]
	global_load_lds_dwordx4 v[0:1], off
	s_mov_b32 m0, s56
	v_lshl_add_u64 v[0:1], s[26:27], 0, v[164:165]
	global_load_lds_dwordx4 v[0:1], off
	s_waitcnt vmcnt(6)
	s_barrier
	s_setprio 1
	v_mfma_scale_f32_16x16x128_f8f6f4 v[60:63], v[234:241], v[16:23], v[60:63], v191, v191 op_sel_hi:[0,0,0]
	v_mfma_scale_f32_16x16x128_f8f6f4 v[56:59], v[242:249], v[16:23], v[56:59], v191, v191 op_sel_hi:[0,0,0]
	v_mfma_scale_f32_16x16x128_f8f6f4 v[52:55], v[234:241], v[24:31], v[52:55], v191, v191 op_sel_hi:[0,0,0]
	v_mfma_scale_f32_16x16x128_f8f6f4 v[48:51], v[242:249], v[24:31], v[48:51], v191, v191 op_sel_hi:[0,0,0]
	v_mfma_scale_f32_16x16x128_f8f6f4 v[44:47], v[234:241], v[178:185], v[44:47], v191, v191 op_sel_hi:[0,0,0]
	v_mfma_scale_f32_16x16x128_f8f6f4 v[40:43], v[242:249], v[178:185], v[40:43], v191, v191 op_sel_hi:[0,0,0]
	v_mfma_scale_f32_16x16x128_f8f6f4 v[36:39], v[234:241], v[218:225], v[36:39], v191, v191 op_sel_hi:[0,0,0]
	v_mfma_scale_f32_16x16x128_f8f6f4 v[32:35], v[242:249], v[218:225], v[32:35], v191, v191 op_sel_hi:[0,0,0]
	s_setprio 0
	s_add_i32 s13, s13, 2
	s_add_u32 s24, s24, 0x100
	s_addc_u32 s25, s25, 0
	s_add_u32 s2, s2, 0x100
	s_addc_u32 s3, s3, 0
	s_cmp_gt_u32 s13, 5
	s_barrier
	s_branch .LBB0_539
.LBB0_538:
	ds_read_b128 v[0:3], v193
	ds_read_b128 v[8:11], v193 offset:2048
	ds_read_b128 v[4:7], v195
	ds_read_b128 v[12:15], v195 offset:2048
	s_add_u32 s15, s24, 0x80
	s_addc_u32 s23, s25, 0
	s_and_b64 s[26:27], s[26:27], exec
	s_cselect_b32 s29, s19, s23
	s_cselect_b32 s28, s18, s15
	s_cselect_b32 s27, s17, s3
	s_cselect_b32 s26, s16, s2
	v_lshl_add_u64 v[16:17], s[24:25], 0, v[168:169]
	s_add_i32 m0, s47, 0xc000
	ds_read_b128 v[218:221], v192
	ds_read_b128 v[226:229], v192 offset:2048
	ds_read_b128 v[222:225], v194
	ds_read_b128 v[230:233], v194 offset:2048
	ds_read_b128 v[234:237], v192 offset:4096
	ds_read_b128 v[242:245], v192 offset:6144
	ds_read_b128 v[238:241], v194 offset:4096
	ds_read_b128 v[246:249], v194 offset:6144
	global_load_lds_dwordx4 v[16:17], off
	s_add_i32 m0, s47, 0xe000
	v_lshl_add_u64 v[16:17], s[24:25], 0, v[174:175]
	global_load_lds_dwordx4 v[16:17], off
	s_waitcnt lgkmcnt(8)
	s_barrier
	s_waitcnt lgkmcnt(0)
	s_setprio 1
	v_mfma_scale_f32_16x16x128_f8f6f4 v[156:159], v[0:7], v[218:225], v[156:159], v191, v191 op_sel_hi:[0,0,0]
	v_mfma_scale_f32_16x16x128_f8f6f4 v[152:155], v[8:15], v[218:225], v[152:155], v191, v191 op_sel_hi:[0,0,0]
	v_mfma_scale_f32_16x16x128_f8f6f4 v[148:151], v[0:7], v[226:233], v[148:151], v191, v191 op_sel_hi:[0,0,0]
	v_mfma_scale_f32_16x16x128_f8f6f4 v[144:147], v[8:15], v[226:233], v[144:147], v191, v191 op_sel_hi:[0,0,0]
	v_mfma_scale_f32_16x16x128_f8f6f4 v[140:143], v[0:7], v[234:241], v[140:143], v191, v191 op_sel_hi:[0,0,0]
	v_mfma_scale_f32_16x16x128_f8f6f4 v[136:139], v[8:15], v[234:241], v[136:139], v191, v191 op_sel_hi:[0,0,0]
	v_mfma_scale_f32_16x16x128_f8f6f4 v[132:135], v[0:7], v[242:249], v[132:135], v191, v191 op_sel_hi:[0,0,0]
	v_mfma_scale_f32_16x16x128_f8f6f4 v[128:131], v[8:15], v[242:249], v[128:131], v191, v191 op_sel_hi:[0,0,0]
	s_setprio 0
	s_barrier
	s_mov_b32 m0, s30
	v_lshl_add_u64 v[182:183], s[26:27], 0, v[162:163]
	ds_read_b128 v[16:19], v193 offset:16384
	ds_read_b128 v[24:27], v193 offset:18432
	ds_read_b128 v[20:23], v195 offset:16384
	ds_read_b128 v[28:31], v195 offset:18432
	global_load_lds_dwordx4 v[182:183], off
	s_mov_b32 m0, s46
	v_lshl_add_u64 v[184:185], s[26:27], 0, v[164:165]
	global_load_lds_dwordx4 v[184:185], off
	s_barrier
	s_waitcnt lgkmcnt(0)
	s_setprio 1
	v_mfma_scale_f32_16x16x128_f8f6f4 v[92:95], v[16:23], v[218:225], v[92:95], v191, v191 op_sel_hi:[0,0,0]
	v_mfma_scale_f32_16x16x128_f8f6f4 v[88:91], v[24:31], v[218:225], v[88:91], v191, v191 op_sel_hi:[0,0,0]
	v_mfma_scale_f32_16x16x128_f8f6f4 v[84:87], v[16:23], v[226:233], v[84:87], v191, v191 op_sel_hi:[0,0,0]
	v_mfma_scale_f32_16x16x128_f8f6f4 v[80:83], v[24:31], v[226:233], v[80:83], v191, v191 op_sel_hi:[0,0,0]
	v_mfma_scale_f32_16x16x128_f8f6f4 v[76:79], v[16:23], v[234:241], v[76:79], v191, v191 op_sel_hi:[0,0,0]
	v_mfma_scale_f32_16x16x128_f8f6f4 v[72:75], v[24:31], v[234:241], v[72:75], v191, v191 op_sel_hi:[0,0,0]
	v_mfma_scale_f32_16x16x128_f8f6f4 v[68:71], v[16:23], v[242:249], v[68:71], v191, v191 op_sel_hi:[0,0,0]
	v_mfma_scale_f32_16x16x128_f8f6f4 v[64:67], v[24:31], v[242:249], v[64:67], v191, v191 op_sel_hi:[0,0,0]
	s_setprio 0
	s_mov_b32 m0, s47
	s_barrier
	ds_read_b128 v[218:221], v192 offset:16384
	ds_read_b128 v[226:229], v192 offset:18432
	ds_read_b128 v[222:225], v194 offset:16384
	ds_read_b128 v[230:233], v194 offset:18432
	ds_read_b128 v[234:237], v192 offset:20480
	ds_read_b128 v[242:245], v192 offset:22528
	ds_read_b128 v[238:241], v194 offset:20480
	ds_read_b128 v[246:249], v194 offset:22528
	global_load_lds_dwordx4 v172, s[28:29]
	s_mov_b32 m0, s83
	v_mov_b32_e32 v187, v173
	global_load_lds_dwordx4 v186, s[28:29]
	s_barrier
	s_waitcnt lgkmcnt(0)
	v_lshl_add_u64 v[188:189], s[28:29], 0, v[172:173]
	v_lshl_add_u64 v[186:187], s[28:29], 0, v[186:187]
	s_setprio 1
	s_waitcnt lgkmcnt(0)
	v_mfma_scale_f32_16x16x128_f8f6f4 v[124:127], v[0:7], v[218:225], v[124:127], v191, v191 op_sel_hi:[0,0,0]
	v_mfma_scale_f32_16x16x128_f8f6f4 v[120:123], v[8:15], v[218:225], v[120:123], v191, v191 op_sel_hi:[0,0,0]
	v_mfma_scale_f32_16x16x128_f8f6f4 v[116:119], v[0:7], v[226:233], v[116:119], v191, v191 op_sel_hi:[0,0,0]
	v_mfma_scale_f32_16x16x128_f8f6f4 v[112:115], v[8:15], v[226:233], v[112:115], v191, v191 op_sel_hi:[0,0,0]
	v_mfma_scale_f32_16x16x128_f8f6f4 v[108:111], v[0:7], v[234:241], v[108:111], v191, v191 op_sel_hi:[0,0,0]
	v_mfma_scale_f32_16x16x128_f8f6f4 v[104:107], v[8:15], v[234:241], v[104:107], v191, v191 op_sel_hi:[0,0,0]
	v_mfma_scale_f32_16x16x128_f8f6f4 v[100:103], v[0:7], v[242:249], v[100:103], v191, v191 op_sel_hi:[0,0,0]
	v_mfma_scale_f32_16x16x128_f8f6f4 v[96:99], v[8:15], v[242:249], v[96:99], v191, v191 op_sel_hi:[0,0,0]
	s_setprio 0
	s_barrier
	s_add_u32 s72, s26, 0x20000
	s_addc_u32 s73, s27, 0
	s_mov_b32 m0, s82
	v_lshl_add_u64 v[0:1], s[72:73], 0, v[162:163]
	global_load_lds_dwordx4 v[0:1], off
	s_mov_b32 m0, s80
	v_lshl_add_u64 v[0:1], s[72:73], 0, v[164:165]
	global_load_lds_dwordx4 v[0:1], off
	s_waitcnt vmcnt(6)
	s_barrier
	s_setprio 1
	v_mfma_scale_f32_16x16x128_f8f6f4 v[60:63], v[16:23], v[218:225], v[60:63], v191, v191 op_sel_hi:[0,0,0]
	v_mfma_scale_f32_16x16x128_f8f6f4 v[56:59], v[24:31], v[218:225], v[56:59], v191, v191 op_sel_hi:[0,0,0]
	v_mfma_scale_f32_16x16x128_f8f6f4 v[52:55], v[16:23], v[226:233], v[52:55], v191, v191 op_sel_hi:[0,0,0]
	v_mfma_scale_f32_16x16x128_f8f6f4 v[48:51], v[24:31], v[226:233], v[48:51], v191, v191 op_sel_hi:[0,0,0]
	v_mfma_scale_f32_16x16x128_f8f6f4 v[44:47], v[16:23], v[234:241], v[44:47], v191, v191 op_sel_hi:[0,0,0]
	v_mfma_scale_f32_16x16x128_f8f6f4 v[40:43], v[24:31], v[234:241], v[40:43], v191, v191 op_sel_hi:[0,0,0]
	v_mfma_scale_f32_16x16x128_f8f6f4 v[36:39], v[16:23], v[242:249], v[36:39], v191, v191 op_sel_hi:[0,0,0]
	v_mfma_scale_f32_16x16x128_f8f6f4 v[32:35], v[24:31], v[242:249], v[32:35], v191, v191 op_sel_hi:[0,0,0]
	s_setprio 0
	s_barrier
	ds_read_b128 v[0:3], v193 offset:32768
	ds_read_b128 v[8:11], v193 offset:34816
	ds_read_b128 v[4:7], v195 offset:32768
	ds_read_b128 v[12:15], v195 offset:34816
	s_mov_b32 m0, s81
	v_lshl_add_u64 v[180:181], s[28:29], 0, v[180:181]
	ds_read_b128 v[16:19], v192 offset:32768
	ds_read_b128 v[24:27], v192 offset:34816
	ds_read_b128 v[20:23], v194 offset:32768
	ds_read_b128 v[28:31], v194 offset:34816
	ds_read_b128 v[218:221], v192 offset:36864
	ds_read_b128 v[226:229], v192 offset:38912
	ds_read_b128 v[222:225], v194 offset:36864
	ds_read_b128 v[230:233], v194 offset:38912
	global_load_lds_dwordx4 v[180:181], off
	s_mov_b32 m0, s50
	v_lshl_add_u64 v[178:179], s[28:29], 0, v[178:179]
	global_load_lds_dwordx4 v[178:179], off
	s_waitcnt lgkmcnt(8)
	s_barrier
	s_waitcnt lgkmcnt(0)
	s_setprio 1
	v_mfma_scale_f32_16x16x128_f8f6f4 v[156:159], v[0:7], v[16:23], v[156:159], v191, v191 op_sel_hi:[0,0,0]
	v_mfma_scale_f32_16x16x128_f8f6f4 v[152:155], v[8:15], v[16:23], v[152:155], v191, v191 op_sel_hi:[0,0,0]
	v_mfma_scale_f32_16x16x128_f8f6f4 v[148:151], v[0:7], v[24:31], v[148:151], v191, v191 op_sel_hi:[0,0,0]
	v_mfma_scale_f32_16x16x128_f8f6f4 v[144:147], v[8:15], v[24:31], v[144:147], v191, v191 op_sel_hi:[0,0,0]
	v_mfma_scale_f32_16x16x128_f8f6f4 v[140:143], v[0:7], v[218:225], v[140:143], v191, v191 op_sel_hi:[0,0,0]
	v_mfma_scale_f32_16x16x128_f8f6f4 v[136:139], v[8:15], v[218:225], v[136:139], v191, v191 op_sel_hi:[0,0,0]
	v_mfma_scale_f32_16x16x128_f8f6f4 v[132:135], v[0:7], v[226:233], v[132:135], v191, v191 op_sel_hi:[0,0,0]
	v_mfma_scale_f32_16x16x128_f8f6f4 v[128:131], v[8:15], v[226:233], v[128:131], v191, v191 op_sel_hi:[0,0,0]
	s_setprio 0
	s_barrier
	s_mov_b32 m0, s51
	v_lshl_add_u64 v[178:179], v[182:183], 0, s[40:41]
	ds_read_b128 v[234:237], v193 offset:49152
	ds_read_b128 v[242:245], v193 offset:51200
	ds_read_b128 v[238:241], v195 offset:49152
	ds_read_b128 v[246:249], v195 offset:51200
	global_load_lds_dwordx4 v[178:179], off
	s_mov_b32 m0, s70
	v_lshl_add_u64 v[178:179], v[184:185], 0, s[40:41]
	global_load_lds_dwordx4 v[178:179], off
	s_barrier
	s_waitcnt lgkmcnt(0)
	s_setprio 1
	v_mfma_scale_f32_16x16x128_f8f6f4 v[92:95], v[234:241], v[16:23], v[92:95], v191, v191 op_sel_hi:[0,0,0]
	v_mfma_scale_f32_16x16x128_f8f6f4 v[88:91], v[242:249], v[16:23], v[88:91], v191, v191 op_sel_hi:[0,0,0]
	v_mfma_scale_f32_16x16x128_f8f6f4 v[84:87], v[234:241], v[24:31], v[84:87], v191, v191 op_sel_hi:[0,0,0]
	v_mfma_scale_f32_16x16x128_f8f6f4 v[80:83], v[242:249], v[24:31], v[80:83], v191, v191 op_sel_hi:[0,0,0]
	v_mfma_scale_f32_16x16x128_f8f6f4 v[76:79], v[234:241], v[218:225], v[76:79], v191, v191 op_sel_hi:[0,0,0]
	v_mfma_scale_f32_16x16x128_f8f6f4 v[72:75], v[242:249], v[218:225], v[72:75], v191, v191 op_sel_hi:[0,0,0]
	v_mfma_scale_f32_16x16x128_f8f6f4 v[68:71], v[234:241], v[226:233], v[68:71], v191, v191 op_sel_hi:[0,0,0]
	v_mfma_scale_f32_16x16x128_f8f6f4 v[64:67], v[242:249], v[226:233], v[64:67], v191, v191 op_sel_hi:[0,0,0]
	s_setprio 0
	s_mov_b32 m0, s71
	v_lshl_add_u64 v[188:189], v[188:189], 0, s[40:41]
	s_barrier
	ds_read_b128 v[16:19], v192 offset:49152
	ds_read_b128 v[24:27], v192 offset:51200
	ds_read_b128 v[20:23], v194 offset:49152
	ds_read_b128 v[28:31], v194 offset:51200
	ds_read_b128 v[178:181], v192 offset:53248
	ds_read_b128 v[218:221], v192 offset:55296
	ds_read_b128 v[182:185], v194 offset:53248
	ds_read_b128 v[222:225], v194 offset:55296
	global_load_lds_dwordx4 v[188:189], off
	s_mov_b32 m0, s87
	v_lshl_add_u64 v[186:187], v[186:187], 0, s[40:41]
	global_load_lds_dwordx4 v[186:187], off
	s_barrier
	s_waitcnt lgkmcnt(0)
	s_setprio 1
	v_mfma_scale_f32_16x16x128_f8f6f4 v[124:127], v[0:7], v[16:23], v[124:127], v191, v191 op_sel_hi:[0,0,0]
	v_mfma_scale_f32_16x16x128_f8f6f4 v[120:123], v[8:15], v[16:23], v[120:123], v191, v191 op_sel_hi:[0,0,0]
	v_mfma_scale_f32_16x16x128_f8f6f4 v[116:119], v[0:7], v[24:31], v[116:119], v191, v191 op_sel_hi:[0,0,0]
	v_mfma_scale_f32_16x16x128_f8f6f4 v[112:115], v[8:15], v[24:31], v[112:115], v191, v191 op_sel_hi:[0,0,0]
	v_mfma_scale_f32_16x16x128_f8f6f4 v[108:111], v[0:7], v[178:185], v[108:111], v191, v191 op_sel_hi:[0,0,0]
	v_mfma_scale_f32_16x16x128_f8f6f4 v[104:107], v[8:15], v[178:185], v[104:107], v191, v191 op_sel_hi:[0,0,0]
	v_mfma_scale_f32_16x16x128_f8f6f4 v[100:103], v[0:7], v[218:225], v[100:103], v191, v191 op_sel_hi:[0,0,0]
	v_mfma_scale_f32_16x16x128_f8f6f4 v[96:99], v[8:15], v[218:225], v[96:99], v191, v191 op_sel_hi:[0,0,0]
	s_setprio 0
	s_barrier
	s_add_u32 s26, s26, 0x20080
	s_addc_u32 s27, s27, 0
	s_mov_b32 m0, s1
	v_lshl_add_u64 v[0:1], s[26:27], 0, v[162:163]
	global_load_lds_dwordx4 v[0:1], off
	s_mov_b32 m0, s56
	v_lshl_add_u64 v[0:1], s[26:27], 0, v[164:165]
	global_load_lds_dwordx4 v[0:1], off
	s_waitcnt vmcnt(6)
	s_barrier
	s_setprio 1
	v_mfma_scale_f32_16x16x128_f8f6f4 v[60:63], v[234:241], v[16:23], v[60:63], v191, v191 op_sel_hi:[0,0,0]
	v_mfma_scale_f32_16x16x128_f8f6f4 v[56:59], v[242:249], v[16:23], v[56:59], v191, v191 op_sel_hi:[0,0,0]
	v_mfma_scale_f32_16x16x128_f8f6f4 v[52:55], v[234:241], v[24:31], v[52:55], v191, v191 op_sel_hi:[0,0,0]
	v_mfma_scale_f32_16x16x128_f8f6f4 v[48:51], v[242:249], v[24:31], v[48:51], v191, v191 op_sel_hi:[0,0,0]
	v_mfma_scale_f32_16x16x128_f8f6f4 v[44:47], v[234:241], v[178:185], v[44:47], v191, v191 op_sel_hi:[0,0,0]
	v_mfma_scale_f32_16x16x128_f8f6f4 v[40:43], v[242:249], v[178:185], v[40:43], v191, v191 op_sel_hi:[0,0,0]
	v_mfma_scale_f32_16x16x128_f8f6f4 v[36:39], v[234:241], v[218:225], v[36:39], v191, v191 op_sel_hi:[0,0,0]
	v_mfma_scale_f32_16x16x128_f8f6f4 v[32:35], v[242:249], v[218:225], v[32:35], v191, v191 op_sel_hi:[0,0,0]
	s_setprio 0
	s_add_i32 s13, s13, 2
	s_add_u32 s24, s24, 0x100
	s_addc_u32 s25, s25, 0
	s_add_u32 s2, s2, 0x100
	s_addc_u32 s3, s3, 0
	s_cmp_gt_u32 s13, 5
	s_barrier
	s_cbranch_scc1 .LBB0_541

.Lpeel_out:
	s_mov_b64 s[28:29], 0
	v_mov_b64_e32 v[136:137], v[132:133]
	v_mov_b64_e32 v[138:139], v[128:129]
	v_mov_b32_e32 v172, v130
	v_mov_b32_e32 v140, v134
	ds_read_b128 v[142:145], v186
	ds_read_b128 v[146:149], v186 offset:1024
	ds_read_b128 v[150:153], v186 offset:2048
	ds_read_b128 v[162:165], v186 offset:3072
	s_add_u32 s30, s26, 0x80
	s_addc_u32 s31, s27, 0
	s_and_b64 s[28:29], s[28:29], exec
	s_cselect_b32 s31, s19, s31
	s_cselect_b32 s30, s18, s30
	s_cselect_b32 s29, s17, s15
	s_cselect_b32 s28, s16, s9
	v_lshl_add_u64 v[154:155], s[26:27], 0, v[128:129]
	s_add_i32 m0, s23, 0xc000
	ds_read_b128 v[166:169], v185
	ds_read_b128 v[174:177], v185 offset:1024
	ds_read_b128 v[178:181], v185 offset:2048
	ds_read_b128 v[204:207], v185 offset:3072
	ds_read_b128 v[208:211], v185 offset:4096
	ds_read_b128 v[214:217], v185 offset:5120
	ds_read_b128 v[218:221], v185 offset:6144
	ds_read_b128 v[222:225], v185 offset:7168
	global_load_lds_dwordx4 v[154:155], off
	s_add_i32 m0, s23, 0xe000
	v_lshl_add_u64 v[154:155], s[26:27], 0, v[132:133]
	global_load_lds_dwordx4 v[154:155], off
	s_waitcnt lgkmcnt(8)
	s_barrier
	s_waitcnt lgkmcnt(0)
	s_setprio 1
	v_mfma_f32_16x16x32_bf16 v[124:127], v[142:145], v[166:169], 0
	v_mfma_f32_16x16x32_bf16 v[120:123], v[150:153], v[166:169], 0
	v_mfma_f32_16x16x32_bf16 v[116:119], v[142:145], v[178:181], 0
	v_mfma_f32_16x16x32_bf16 v[112:115], v[150:153], v[178:181], 0
	v_mfma_f32_16x16x32_bf16 v[108:111], v[142:145], v[208:211], 0
	v_mfma_f32_16x16x32_bf16 v[104:107], v[150:153], v[208:211], 0
	v_mfma_f32_16x16x32_bf16 v[100:103], v[142:145], v[218:221], 0
	v_mfma_f32_16x16x32_bf16 v[96:99], v[150:153], v[218:221], 0
	v_mfma_f32_16x16x32_bf16 v[124:127], v[146:149], v[174:177], v[124:127]
	v_mfma_f32_16x16x32_bf16 v[120:123], v[162:165], v[174:177], v[120:123]
	v_mfma_f32_16x16x32_bf16 v[116:119], v[146:149], v[204:207], v[116:119]
	v_mfma_f32_16x16x32_bf16 v[112:115], v[162:165], v[204:207], v[112:115]
	v_mfma_f32_16x16x32_bf16 v[108:111], v[146:149], v[214:217], v[108:111]
	v_mfma_f32_16x16x32_bf16 v[104:107], v[162:165], v[214:217], v[104:107]
	v_mfma_f32_16x16x32_bf16 v[100:103], v[146:149], v[222:225], v[100:103]
	v_mfma_f32_16x16x32_bf16 v[96:99], v[162:165], v[222:225], v[96:99]
	s_setprio 0
	s_barrier
	s_mov_b32 m0, s25
	v_lshl_add_u64 v[170:171], s[28:29], 0, v[158:159]
	ds_read_b128 v[226:229], v186 offset:16384
	ds_read_b128 v[230:233], v186 offset:17408
	ds_read_b128 v[234:237], v186 offset:18432
	ds_read_b128 v[238:241], v186 offset:19456
	global_load_lds_dwordx4 v[170:171], off
	s_mov_b32 m0, s51
	v_lshl_add_u64 v[182:183], s[28:29], 0, v[160:161]
	global_load_lds_dwordx4 v[182:183], off
	s_barrier
	s_waitcnt lgkmcnt(0)
	s_setprio 1
	v_mfma_f32_16x16x32_bf16 v[68:71], v[226:229], v[166:169], 0
	v_mfma_f32_16x16x32_bf16 v[64:67], v[234:237], v[166:169], 0
	v_mfma_f32_16x16x32_bf16 v[52:55], v[226:229], v[178:181], 0
	v_mfma_f32_16x16x32_bf16 v[48:51], v[234:237], v[178:181], 0
	v_mfma_f32_16x16x32_bf16 v[44:47], v[226:229], v[208:211], 0
	v_mfma_f32_16x16x32_bf16 v[40:43], v[234:237], v[208:211], 0
	v_mfma_f32_16x16x32_bf16 v[36:39], v[226:229], v[218:221], 0
	v_mfma_f32_16x16x32_bf16 v[32:35], v[234:237], v[218:221], 0
	v_mfma_f32_16x16x32_bf16 v[68:71], v[230:233], v[174:177], v[68:71]
	v_mfma_f32_16x16x32_bf16 v[64:67], v[238:241], v[174:177], v[64:67]
	v_mfma_f32_16x16x32_bf16 v[52:55], v[230:233], v[204:207], v[52:55]
	v_mfma_f32_16x16x32_bf16 v[48:51], v[238:241], v[204:207], v[48:51]
	v_mfma_f32_16x16x32_bf16 v[44:47], v[230:233], v[214:217], v[44:47]
	v_mfma_f32_16x16x32_bf16 v[40:43], v[238:241], v[214:217], v[40:43]
	v_mfma_f32_16x16x32_bf16 v[36:39], v[230:233], v[222:225], v[36:39]
	v_mfma_f32_16x16x32_bf16 v[32:35], v[238:241], v[222:225], v[32:35]
	s_setprio 0
	s_mov_b32 m0, s23
	s_barrier
	ds_read_b128 v[166:169], v185 offset:16384
	ds_read_b128 v[174:177], v185 offset:17408
	ds_read_b128 v[178:181], v185 offset:18432
	ds_read_b128 v[204:207], v185 offset:19456
	ds_read_b128 v[208:211], v185 offset:20480
	ds_read_b128 v[214:217], v185 offset:21504
	ds_read_b128 v[218:221], v185 offset:22528
	ds_read_b128 v[222:225], v185 offset:23552
	global_load_lds_dwordx4 v172, s[30:31]
	s_mov_b32 m0, s56
	v_mov_b32_e32 v141, v173
	global_load_lds_dwordx4 v140, s[30:31]
	s_barrier
	s_waitcnt lgkmcnt(0)
	v_lshl_add_u64 v[196:197], s[30:31], 0, v[172:173]
	v_lshl_add_u64 v[242:243], s[30:31], 0, v[140:141]
	s_setprio 1
	s_waitcnt lgkmcnt(0)
	v_mfma_f32_16x16x32_bf16 v[92:95], v[142:145], v[166:169], 0
	v_mfma_f32_16x16x32_bf16 v[88:91], v[150:153], v[166:169], 0
	v_mfma_f32_16x16x32_bf16 v[84:87], v[142:145], v[178:181], 0
	v_mfma_f32_16x16x32_bf16 v[80:83], v[150:153], v[178:181], 0
	v_mfma_f32_16x16x32_bf16 v[76:79], v[142:145], v[208:211], 0
	v_mfma_f32_16x16x32_bf16 v[72:75], v[150:153], v[208:211], 0
	v_mfma_f32_16x16x32_bf16 v[60:63], v[142:145], v[218:221], 0
	v_mfma_f32_16x16x32_bf16 v[56:59], v[150:153], v[218:221], 0
	v_mfma_f32_16x16x32_bf16 v[92:95], v[146:149], v[174:177], v[92:95]
	v_mfma_f32_16x16x32_bf16 v[88:91], v[162:165], v[174:177], v[88:91]
	v_mfma_f32_16x16x32_bf16 v[84:87], v[146:149], v[204:207], v[84:87]
	v_mfma_f32_16x16x32_bf16 v[80:83], v[162:165], v[204:207], v[80:83]
	v_mfma_f32_16x16x32_bf16 v[76:79], v[146:149], v[214:217], v[76:79]
	v_mfma_f32_16x16x32_bf16 v[72:75], v[162:165], v[214:217], v[72:75]
	v_mfma_f32_16x16x32_bf16 v[60:63], v[146:149], v[222:225], v[60:63]
	v_mfma_f32_16x16x32_bf16 v[56:59], v[162:165], v[222:225], v[56:59]
	s_setprio 0
	s_barrier
	s_add_u32 s94, s28, 0x40000
	s_addc_u32 s95, s29, 0
	s_mov_b32 m0, s65
	v_lshl_add_u64 v[140:141], s[94:95], 0, v[158:159]
	global_load_lds_dwordx4 v[140:141], off
	s_mov_b32 m0, s70
	v_lshl_add_u64 v[140:141], s[94:95], 0, v[160:161]
	global_load_lds_dwordx4 v[140:141], off
	s_waitcnt vmcnt(6)
	s_barrier
	s_setprio 1
	v_mfma_f32_16x16x32_bf16 v[28:31], v[226:229], v[166:169], 0
	v_mfma_f32_16x16x32_bf16 v[24:27], v[234:237], v[166:169], 0
	v_mfma_f32_16x16x32_bf16 v[20:23], v[226:229], v[178:181], 0
	v_mfma_f32_16x16x32_bf16 v[16:19], v[234:237], v[178:181], 0
	v_mfma_f32_16x16x32_bf16 v[12:15], v[226:229], v[208:211], 0
	v_mfma_f32_16x16x32_bf16 v[8:11], v[234:237], v[208:211], 0
	v_mfma_f32_16x16x32_bf16 v[4:7], v[226:229], v[218:221], 0
	v_mfma_f32_16x16x32_bf16 v[0:3], v[234:237], v[218:221], 0
	v_mfma_f32_16x16x32_bf16 v[28:31], v[230:233], v[174:177], v[28:31]
	v_mfma_f32_16x16x32_bf16 v[24:27], v[238:241], v[174:177], v[24:27]
	v_mfma_f32_16x16x32_bf16 v[20:23], v[230:233], v[204:207], v[20:23]
	v_mfma_f32_16x16x32_bf16 v[16:19], v[238:241], v[204:207], v[16:19]
	v_mfma_f32_16x16x32_bf16 v[12:15], v[230:233], v[214:217], v[12:15]
	v_mfma_f32_16x16x32_bf16 v[8:11], v[238:241], v[214:217], v[8:11]
	v_mfma_f32_16x16x32_bf16 v[4:7], v[230:233], v[222:225], v[4:7]
	v_mfma_f32_16x16x32_bf16 v[0:3], v[238:241], v[222:225], v[0:3]
	s_setprio 0
	s_barrier
	ds_read_b128 v[140:143], v186 offset:32768
	ds_read_b128 v[144:147], v186 offset:33792
	ds_read_b128 v[148:151], v186 offset:34816
	ds_read_b128 v[152:155], v186 offset:35840
	s_mov_b32 m0, s71
	v_lshl_add_u64 v[138:139], s[30:31], 0, v[138:139]
	ds_read_b128 v[162:165], v185 offset:32768
	ds_read_b128 v[166:169], v185 offset:33792
	ds_read_b128 v[174:177], v185 offset:34816
	ds_read_b128 v[178:181], v185 offset:35840
	ds_read_b128 v[204:207], v185 offset:36864
	ds_read_b128 v[208:211], v185 offset:37888
	ds_read_b128 v[214:217], v185 offset:38912
	ds_read_b128 v[218:221], v185 offset:39936
	global_load_lds_dwordx4 v[138:139], off
	s_mov_b32 m0, s80
	v_lshl_add_u64 v[136:137], s[30:31], 0, v[136:137]
	global_load_lds_dwordx4 v[136:137], off
	s_waitcnt lgkmcnt(8)
	s_barrier
	s_waitcnt lgkmcnt(0)
	s_setprio 1
	v_mfma_f32_16x16x32_bf16 v[124:127], v[140:143], v[162:165], v[124:127]
	v_mfma_f32_16x16x32_bf16 v[120:123], v[148:151], v[162:165], v[120:123]
	v_mfma_f32_16x16x32_bf16 v[116:119], v[140:143], v[174:177], v[116:119]
	v_mfma_f32_16x16x32_bf16 v[112:115], v[148:151], v[174:177], v[112:115]
	v_mfma_f32_16x16x32_bf16 v[108:111], v[140:143], v[204:207], v[108:111]
	v_mfma_f32_16x16x32_bf16 v[104:107], v[148:151], v[204:207], v[104:107]
	v_mfma_f32_16x16x32_bf16 v[100:103], v[140:143], v[214:217], v[100:103]
	v_mfma_f32_16x16x32_bf16 v[96:99], v[148:151], v[214:217], v[96:99]
	v_mfma_f32_16x16x32_bf16 v[124:127], v[144:147], v[166:169], v[124:127]
	v_mfma_f32_16x16x32_bf16 v[120:123], v[152:155], v[166:169], v[120:123]
	v_mfma_f32_16x16x32_bf16 v[116:119], v[144:147], v[178:181], v[116:119]
	v_mfma_f32_16x16x32_bf16 v[112:115], v[152:155], v[178:181], v[112:115]
	v_mfma_f32_16x16x32_bf16 v[108:111], v[144:147], v[208:211], v[108:111]
	v_mfma_f32_16x16x32_bf16 v[104:107], v[152:155], v[208:211], v[104:107]
	v_mfma_f32_16x16x32_bf16 v[100:103], v[144:147], v[218:221], v[100:103]
	v_mfma_f32_16x16x32_bf16 v[96:99], v[152:155], v[218:221], v[96:99]
	s_setprio 0
	s_barrier
	s_mov_b32 m0, s81
	v_lshl_add_u64 v[170:171], v[170:171], 0, s[40:41]
	ds_read_b128 v[136:139], v186 offset:49152
	ds_read_b128 v[222:225], v186 offset:50176
	ds_read_b128 v[226:229], v186 offset:51200
	ds_read_b128 v[230:233], v186 offset:52224
	global_load_lds_dwordx4 v[170:171], off
	s_mov_b32 m0, s82
	v_lshl_add_u64 v[170:171], v[182:183], 0, s[40:41]
	global_load_lds_dwordx4 v[170:171], off
	s_barrier
	s_waitcnt lgkmcnt(0)
	s_setprio 1
	v_mfma_f32_16x16x32_bf16 v[68:71], v[136:139], v[162:165], v[68:71]
	v_mfma_f32_16x16x32_bf16 v[64:67], v[226:229], v[162:165], v[64:67]
	v_mfma_f32_16x16x32_bf16 v[52:55], v[136:139], v[174:177], v[52:55]
	v_mfma_f32_16x16x32_bf16 v[48:51], v[226:229], v[174:177], v[48:51]
	v_mfma_f32_16x16x32_bf16 v[44:47], v[136:139], v[204:207], v[44:47]
	v_mfma_f32_16x16x32_bf16 v[40:43], v[226:229], v[204:207], v[40:43]
	v_mfma_f32_16x16x32_bf16 v[36:39], v[136:139], v[214:217], v[36:39]
	v_mfma_f32_16x16x32_bf16 v[32:35], v[226:229], v[214:217], v[32:35]
	v_mfma_f32_16x16x32_bf16 v[68:71], v[222:225], v[166:169], v[68:71]
	v_mfma_f32_16x16x32_bf16 v[64:67], v[230:233], v[166:169], v[64:67]
	v_mfma_f32_16x16x32_bf16 v[52:55], v[222:225], v[178:181], v[52:55]
	v_mfma_f32_16x16x32_bf16 v[48:51], v[230:233], v[178:181], v[48:51]
	v_mfma_f32_16x16x32_bf16 v[44:47], v[222:225], v[208:211], v[44:47]
	v_mfma_f32_16x16x32_bf16 v[40:43], v[230:233], v[208:211], v[40:43]
	v_mfma_f32_16x16x32_bf16 v[36:39], v[222:225], v[218:221], v[36:39]
	v_mfma_f32_16x16x32_bf16 v[32:35], v[230:233], v[218:221], v[32:35]
	s_setprio 0
	s_mov_b32 m0, s83
	v_lshl_add_u64 v[170:171], v[196:197], 0, s[40:41]
	s_barrier
	ds_read_b128 v[162:165], v185 offset:49152
	ds_read_b128 v[166:169], v185 offset:50176
	ds_read_b128 v[174:177], v185 offset:51200
	ds_read_b128 v[178:181], v185 offset:52224
	ds_read_b128 v[204:207], v185 offset:53248
	ds_read_b128 v[208:211], v185 offset:54272
	ds_read_b128 v[214:217], v185 offset:55296
	ds_read_b128 v[218:221], v185 offset:56320
	global_load_lds_dwordx4 v[170:171], off
	s_mov_b32 m0, s85
	v_lshl_add_u64 v[170:171], v[242:243], 0, s[40:41]
	global_load_lds_dwordx4 v[170:171], off
	s_barrier
	s_waitcnt lgkmcnt(0)
	s_setprio 1
	v_mfma_f32_16x16x32_bf16 v[92:95], v[140:143], v[162:165], v[92:95]
	v_mfma_f32_16x16x32_bf16 v[88:91], v[148:151], v[162:165], v[88:91]
	v_mfma_f32_16x16x32_bf16 v[84:87], v[140:143], v[174:177], v[84:87]
	v_mfma_f32_16x16x32_bf16 v[80:83], v[148:151], v[174:177], v[80:83]
	v_mfma_f32_16x16x32_bf16 v[76:79], v[140:143], v[204:207], v[76:79]
	v_mfma_f32_16x16x32_bf16 v[72:75], v[148:151], v[204:207], v[72:75]
	v_mfma_f32_16x16x32_bf16 v[60:63], v[140:143], v[214:217], v[60:63]
	v_mfma_f32_16x16x32_bf16 v[56:59], v[148:151], v[214:217], v[56:59]
	v_mfma_f32_16x16x32_bf16 v[92:95], v[144:147], v[166:169], v[92:95]
	v_mfma_f32_16x16x32_bf16 v[88:91], v[152:155], v[166:169], v[88:91]
	v_mfma_f32_16x16x32_bf16 v[84:87], v[144:147], v[178:181], v[84:87]
	v_mfma_f32_16x16x32_bf16 v[80:83], v[152:155], v[178:181], v[80:83]
	v_mfma_f32_16x16x32_bf16 v[76:79], v[144:147], v[208:211], v[76:79]
	v_mfma_f32_16x16x32_bf16 v[72:75], v[152:155], v[208:211], v[72:75]
	v_mfma_f32_16x16x32_bf16 v[60:63], v[144:147], v[218:221], v[60:63]
	v_mfma_f32_16x16x32_bf16 v[56:59], v[152:155], v[218:221], v[56:59]
	s_setprio 0
	s_barrier
	s_add_u32 s28, s28, 0x40080
	s_addc_u32 s29, s29, 0
	s_mov_b32 m0, s87
	v_lshl_add_u64 v[140:141], s[28:29], 0, v[158:159]
	global_load_lds_dwordx4 v[140:141], off
	s_mov_b32 m0, s44
	v_lshl_add_u64 v[140:141], s[28:29], 0, v[160:161]
	global_load_lds_dwordx4 v[140:141], off
	s_waitcnt vmcnt(6)
	s_barrier
	s_setprio 1
	v_mfma_f32_16x16x32_bf16 v[28:31], v[136:139], v[162:165], v[28:31]
	v_mfma_f32_16x16x32_bf16 v[24:27], v[226:229], v[162:165], v[24:27]
	v_mfma_f32_16x16x32_bf16 v[20:23], v[136:139], v[174:177], v[20:23]
	v_mfma_f32_16x16x32_bf16 v[16:19], v[226:229], v[174:177], v[16:19]
	v_mfma_f32_16x16x32_bf16 v[12:15], v[136:139], v[204:207], v[12:15]
	v_mfma_f32_16x16x32_bf16 v[8:11], v[226:229], v[204:207], v[8:11]
	v_mfma_f32_16x16x32_bf16 v[4:7], v[136:139], v[214:217], v[4:7]
	v_mfma_f32_16x16x32_bf16 v[0:3], v[226:229], v[214:217], v[0:3]
	v_mfma_f32_16x16x32_bf16 v[28:31], v[222:225], v[166:169], v[28:31]
	v_mfma_f32_16x16x32_bf16 v[24:27], v[230:233], v[166:169], v[24:27]
	v_mfma_f32_16x16x32_bf16 v[20:23], v[222:225], v[178:181], v[20:23]
	v_mfma_f32_16x16x32_bf16 v[16:19], v[230:233], v[178:181], v[16:19]
	v_mfma_f32_16x16x32_bf16 v[12:15], v[222:225], v[208:211], v[12:15]
	v_mfma_f32_16x16x32_bf16 v[8:11], v[230:233], v[208:211], v[8:11]
	v_mfma_f32_16x16x32_bf16 v[4:7], v[222:225], v[218:221], v[4:7]
	v_mfma_f32_16x16x32_bf16 v[0:3], v[230:233], v[218:221], v[0:3]
	s_setprio 0
	s_add_i32 vcc_lo, vcc_lo, 2
	s_add_u32 s26, s26, 0x100
	s_addc_u32 s27, s27, 0
	s_add_u32 s9, s9, 0x100
	s_addc_u32 s15, s15, 0
	s_cmp_gt_u32 vcc_lo, 13
	s_barrier
	s_branch .LBB0_1320
.LBB0_1319:
	ds_read_b128 v[142:145], v186
	ds_read_b128 v[146:149], v186 offset:1024
	ds_read_b128 v[150:153], v186 offset:2048
	ds_read_b128 v[162:165], v186 offset:3072
	s_add_u32 s30, s26, 0x80
	s_addc_u32 s31, s27, 0
	s_and_b64 s[28:29], s[28:29], exec
	s_cselect_b32 s31, s19, s31
	s_cselect_b32 s30, s18, s30
	s_cselect_b32 s29, s17, s15
	s_cselect_b32 s28, s16, s9
	v_lshl_add_u64 v[154:155], s[26:27], 0, v[128:129]
	s_add_i32 m0, s23, 0xc000
	ds_read_b128 v[166:169], v185
	ds_read_b128 v[174:177], v185 offset:1024
	ds_read_b128 v[178:181], v185 offset:2048
	ds_read_b128 v[204:207], v185 offset:3072
	ds_read_b128 v[208:211], v185 offset:4096
	ds_read_b128 v[214:217], v185 offset:5120
	ds_read_b128 v[218:221], v185 offset:6144
	ds_read_b128 v[222:225], v185 offset:7168
	global_load_lds_dwordx4 v[154:155], off
	s_add_i32 m0, s23, 0xe000
	v_lshl_add_u64 v[154:155], s[26:27], 0, v[132:133]
	global_load_lds_dwordx4 v[154:155], off
	s_waitcnt lgkmcnt(8)
	s_barrier
	s_waitcnt lgkmcnt(0)
	s_setprio 1
	v_mfma_f32_16x16x32_bf16 v[124:127], v[142:145], v[166:169], v[124:127]
	v_mfma_f32_16x16x32_bf16 v[120:123], v[150:153], v[166:169], v[120:123]
	v_mfma_f32_16x16x32_bf16 v[116:119], v[142:145], v[178:181], v[116:119]
	v_mfma_f32_16x16x32_bf16 v[112:115], v[150:153], v[178:181], v[112:115]
	v_mfma_f32_16x16x32_bf16 v[108:111], v[142:145], v[208:211], v[108:111]
	v_mfma_f32_16x16x32_bf16 v[104:107], v[150:153], v[208:211], v[104:107]
	v_mfma_f32_16x16x32_bf16 v[100:103], v[142:145], v[218:221], v[100:103]
	v_mfma_f32_16x16x32_bf16 v[96:99], v[150:153], v[218:221], v[96:99]
	v_mfma_f32_16x16x32_bf16 v[124:127], v[146:149], v[174:177], v[124:127]
	v_mfma_f32_16x16x32_bf16 v[120:123], v[162:165], v[174:177], v[120:123]
	v_mfma_f32_16x16x32_bf16 v[116:119], v[146:149], v[204:207], v[116:119]
	v_mfma_f32_16x16x32_bf16 v[112:115], v[162:165], v[204:207], v[112:115]
	v_mfma_f32_16x16x32_bf16 v[108:111], v[146:149], v[214:217], v[108:111]
	v_mfma_f32_16x16x32_bf16 v[104:107], v[162:165], v[214:217], v[104:107]
	v_mfma_f32_16x16x32_bf16 v[100:103], v[146:149], v[222:225], v[100:103]
	v_mfma_f32_16x16x32_bf16 v[96:99], v[162:165], v[222:225], v[96:99]
	s_setprio 0
	s_barrier
	s_mov_b32 m0, s25
	v_lshl_add_u64 v[170:171], s[28:29], 0, v[158:159]
	ds_read_b128 v[226:229], v186 offset:16384
	ds_read_b128 v[230:233], v186 offset:17408
	ds_read_b128 v[234:237], v186 offset:18432
	ds_read_b128 v[238:241], v186 offset:19456
	global_load_lds_dwordx4 v[170:171], off
	s_mov_b32 m0, s51
	v_lshl_add_u64 v[182:183], s[28:29], 0, v[160:161]
	global_load_lds_dwordx4 v[182:183], off
	s_barrier
	s_waitcnt lgkmcnt(0)
	s_setprio 1
	v_mfma_f32_16x16x32_bf16 v[68:71], v[226:229], v[166:169], v[68:71]
	v_mfma_f32_16x16x32_bf16 v[64:67], v[234:237], v[166:169], v[64:67]
	v_mfma_f32_16x16x32_bf16 v[52:55], v[226:229], v[178:181], v[52:55]
	v_mfma_f32_16x16x32_bf16 v[48:51], v[234:237], v[178:181], v[48:51]
	v_mfma_f32_16x16x32_bf16 v[44:47], v[226:229], v[208:211], v[44:47]
	v_mfma_f32_16x16x32_bf16 v[40:43], v[234:237], v[208:211], v[40:43]
	v_mfma_f32_16x16x32_bf16 v[36:39], v[226:229], v[218:221], v[36:39]
	v_mfma_f32_16x16x32_bf16 v[32:35], v[234:237], v[218:221], v[32:35]
	v_mfma_f32_16x16x32_bf16 v[68:71], v[230:233], v[174:177], v[68:71]
	v_mfma_f32_16x16x32_bf16 v[64:67], v[238:241], v[174:177], v[64:67]
	v_mfma_f32_16x16x32_bf16 v[52:55], v[230:233], v[204:207], v[52:55]
	v_mfma_f32_16x16x32_bf16 v[48:51], v[238:241], v[204:207], v[48:51]
	v_mfma_f32_16x16x32_bf16 v[44:47], v[230:233], v[214:217], v[44:47]
	v_mfma_f32_16x16x32_bf16 v[40:43], v[238:241], v[214:217], v[40:43]
	v_mfma_f32_16x16x32_bf16 v[36:39], v[230:233], v[222:225], v[36:39]
	v_mfma_f32_16x16x32_bf16 v[32:35], v[238:241], v[222:225], v[32:35]
	s_setprio 0
	s_mov_b32 m0, s23
	s_barrier
	ds_read_b128 v[166:169], v185 offset:16384
	ds_read_b128 v[174:177], v185 offset:17408
	ds_read_b128 v[178:181], v185 offset:18432
	ds_read_b128 v[204:207], v185 offset:19456
	ds_read_b128 v[208:211], v185 offset:20480
	ds_read_b128 v[214:217], v185 offset:21504
	ds_read_b128 v[218:221], v185 offset:22528
	ds_read_b128 v[222:225], v185 offset:23552
	global_load_lds_dwordx4 v172, s[30:31]
	s_mov_b32 m0, s56
	v_mov_b32_e32 v141, v173
	global_load_lds_dwordx4 v140, s[30:31]
	s_barrier
	s_waitcnt lgkmcnt(0)
	v_lshl_add_u64 v[196:197], s[30:31], 0, v[172:173]
	v_lshl_add_u64 v[242:243], s[30:31], 0, v[140:141]
	s_setprio 1
	s_waitcnt lgkmcnt(0)
	v_mfma_f32_16x16x32_bf16 v[92:95], v[142:145], v[166:169], v[92:95]
	v_mfma_f32_16x16x32_bf16 v[88:91], v[150:153], v[166:169], v[88:91]
	v_mfma_f32_16x16x32_bf16 v[84:87], v[142:145], v[178:181], v[84:87]
	v_mfma_f32_16x16x32_bf16 v[80:83], v[150:153], v[178:181], v[80:83]
	v_mfma_f32_16x16x32_bf16 v[76:79], v[142:145], v[208:211], v[76:79]
	v_mfma_f32_16x16x32_bf16 v[72:75], v[150:153], v[208:211], v[72:75]
	v_mfma_f32_16x16x32_bf16 v[60:63], v[142:145], v[218:221], v[60:63]
	v_mfma_f32_16x16x32_bf16 v[56:59], v[150:153], v[218:221], v[56:59]
	v_mfma_f32_16x16x32_bf16 v[92:95], v[146:149], v[174:177], v[92:95]
	v_mfma_f32_16x16x32_bf16 v[88:91], v[162:165], v[174:177], v[88:91]
	v_mfma_f32_16x16x32_bf16 v[84:87], v[146:149], v[204:207], v[84:87]
	v_mfma_f32_16x16x32_bf16 v[80:83], v[162:165], v[204:207], v[80:83]
	v_mfma_f32_16x16x32_bf16 v[76:79], v[146:149], v[214:217], v[76:79]
	v_mfma_f32_16x16x32_bf16 v[72:75], v[162:165], v[214:217], v[72:75]
	v_mfma_f32_16x16x32_bf16 v[60:63], v[146:149], v[222:225], v[60:63]
	v_mfma_f32_16x16x32_bf16 v[56:59], v[162:165], v[222:225], v[56:59]
	s_setprio 0
	s_barrier
	s_add_u32 s94, s28, 0x40000
	s_addc_u32 s95, s29, 0
	s_mov_b32 m0, s65
	v_lshl_add_u64 v[140:141], s[94:95], 0, v[158:159]
	global_load_lds_dwordx4 v[140:141], off
	s_mov_b32 m0, s70
	v_lshl_add_u64 v[140:141], s[94:95], 0, v[160:161]
	global_load_lds_dwordx4 v[140:141], off
	s_waitcnt vmcnt(6)
	s_barrier
	s_setprio 1
	v_mfma_f32_16x16x32_bf16 v[28:31], v[226:229], v[166:169], v[28:31]
	v_mfma_f32_16x16x32_bf16 v[24:27], v[234:237], v[166:169], v[24:27]
	v_mfma_f32_16x16x32_bf16 v[20:23], v[226:229], v[178:181], v[20:23]
	v_mfma_f32_16x16x32_bf16 v[16:19], v[234:237], v[178:181], v[16:19]
	v_mfma_f32_16x16x32_bf16 v[12:15], v[226:229], v[208:211], v[12:15]
	v_mfma_f32_16x16x32_bf16 v[8:11], v[234:237], v[208:211], v[8:11]
	v_mfma_f32_16x16x32_bf16 v[4:7], v[226:229], v[218:221], v[4:7]
	v_mfma_f32_16x16x32_bf16 v[0:3], v[234:237], v[218:221], v[0:3]
	v_mfma_f32_16x16x32_bf16 v[28:31], v[230:233], v[174:177], v[28:31]
	v_mfma_f32_16x16x32_bf16 v[24:27], v[238:241], v[174:177], v[24:27]
	v_mfma_f32_16x16x32_bf16 v[20:23], v[230:233], v[204:207], v[20:23]
	v_mfma_f32_16x16x32_bf16 v[16:19], v[238:241], v[204:207], v[16:19]
	v_mfma_f32_16x16x32_bf16 v[12:15], v[230:233], v[214:217], v[12:15]
	v_mfma_f32_16x16x32_bf16 v[8:11], v[238:241], v[214:217], v[8:11]
	v_mfma_f32_16x16x32_bf16 v[4:7], v[230:233], v[222:225], v[4:7]
	v_mfma_f32_16x16x32_bf16 v[0:3], v[238:241], v[222:225], v[0:3]
	s_setprio 0
	s_barrier
	ds_read_b128 v[140:143], v186 offset:32768
	ds_read_b128 v[144:147], v186 offset:33792
	ds_read_b128 v[148:151], v186 offset:34816
	ds_read_b128 v[152:155], v186 offset:35840
	s_mov_b32 m0, s71
	v_lshl_add_u64 v[138:139], s[30:31], 0, v[138:139]
	ds_read_b128 v[162:165], v185 offset:32768
	ds_read_b128 v[166:169], v185 offset:33792
	ds_read_b128 v[174:177], v185 offset:34816
	ds_read_b128 v[178:181], v185 offset:35840
	ds_read_b128 v[204:207], v185 offset:36864
	ds_read_b128 v[208:211], v185 offset:37888
	ds_read_b128 v[214:217], v185 offset:38912
	ds_read_b128 v[218:221], v185 offset:39936
	global_load_lds_dwordx4 v[138:139], off
	s_mov_b32 m0, s80
	v_lshl_add_u64 v[136:137], s[30:31], 0, v[136:137]
	global_load_lds_dwordx4 v[136:137], off
	s_waitcnt lgkmcnt(8)
	s_barrier
	s_waitcnt lgkmcnt(0)
	s_setprio 1
	v_mfma_f32_16x16x32_bf16 v[124:127], v[140:143], v[162:165], v[124:127]
	v_mfma_f32_16x16x32_bf16 v[120:123], v[148:151], v[162:165], v[120:123]
	v_mfma_f32_16x16x32_bf16 v[116:119], v[140:143], v[174:177], v[116:119]
	v_mfma_f32_16x16x32_bf16 v[112:115], v[148:151], v[174:177], v[112:115]
	v_mfma_f32_16x16x32_bf16 v[108:111], v[140:143], v[204:207], v[108:111]
	v_mfma_f32_16x16x32_bf16 v[104:107], v[148:151], v[204:207], v[104:107]
	v_mfma_f32_16x16x32_bf16 v[100:103], v[140:143], v[214:217], v[100:103]
	v_mfma_f32_16x16x32_bf16 v[96:99], v[148:151], v[214:217], v[96:99]
	v_mfma_f32_16x16x32_bf16 v[124:127], v[144:147], v[166:169], v[124:127]
	v_mfma_f32_16x16x32_bf16 v[120:123], v[152:155], v[166:169], v[120:123]
	v_mfma_f32_16x16x32_bf16 v[116:119], v[144:147], v[178:181], v[116:119]
	v_mfma_f32_16x16x32_bf16 v[112:115], v[152:155], v[178:181], v[112:115]
	v_mfma_f32_16x16x32_bf16 v[108:111], v[144:147], v[208:211], v[108:111]
	v_mfma_f32_16x16x32_bf16 v[104:107], v[152:155], v[208:211], v[104:107]
	v_mfma_f32_16x16x32_bf16 v[100:103], v[144:147], v[218:221], v[100:103]
	v_mfma_f32_16x16x32_bf16 v[96:99], v[152:155], v[218:221], v[96:99]
	s_setprio 0
	s_barrier
	s_mov_b32 m0, s81
	v_lshl_add_u64 v[170:171], v[170:171], 0, s[40:41]
	ds_read_b128 v[136:139], v186 offset:49152
	ds_read_b128 v[222:225], v186 offset:50176
	ds_read_b128 v[226:229], v186 offset:51200
	ds_read_b128 v[230:233], v186 offset:52224
	global_load_lds_dwordx4 v[170:171], off
	s_mov_b32 m0, s82
	v_lshl_add_u64 v[170:171], v[182:183], 0, s[40:41]
	global_load_lds_dwordx4 v[170:171], off
	s_barrier
	s_waitcnt lgkmcnt(0)
	s_setprio 1
	v_mfma_f32_16x16x32_bf16 v[68:71], v[136:139], v[162:165], v[68:71]
	v_mfma_f32_16x16x32_bf16 v[64:67], v[226:229], v[162:165], v[64:67]
	v_mfma_f32_16x16x32_bf16 v[52:55], v[136:139], v[174:177], v[52:55]
	v_mfma_f32_16x16x32_bf16 v[48:51], v[226:229], v[174:177], v[48:51]
	v_mfma_f32_16x16x32_bf16 v[44:47], v[136:139], v[204:207], v[44:47]
	v_mfma_f32_16x16x32_bf16 v[40:43], v[226:229], v[204:207], v[40:43]
	v_mfma_f32_16x16x32_bf16 v[36:39], v[136:139], v[214:217], v[36:39]
	v_mfma_f32_16x16x32_bf16 v[32:35], v[226:229], v[214:217], v[32:35]
	v_mfma_f32_16x16x32_bf16 v[68:71], v[222:225], v[166:169], v[68:71]
	v_mfma_f32_16x16x32_bf16 v[64:67], v[230:233], v[166:169], v[64:67]
	v_mfma_f32_16x16x32_bf16 v[52:55], v[222:225], v[178:181], v[52:55]
	v_mfma_f32_16x16x32_bf16 v[48:51], v[230:233], v[178:181], v[48:51]
	v_mfma_f32_16x16x32_bf16 v[44:47], v[222:225], v[208:211], v[44:47]
	v_mfma_f32_16x16x32_bf16 v[40:43], v[230:233], v[208:211], v[40:43]
	v_mfma_f32_16x16x32_bf16 v[36:39], v[222:225], v[218:221], v[36:39]
	v_mfma_f32_16x16x32_bf16 v[32:35], v[230:233], v[218:221], v[32:35]
	s_setprio 0
	s_mov_b32 m0, s83
	v_lshl_add_u64 v[170:171], v[196:197], 0, s[40:41]
	s_barrier
	ds_read_b128 v[162:165], v185 offset:49152
	ds_read_b128 v[166:169], v185 offset:50176
	ds_read_b128 v[174:177], v185 offset:51200
	ds_read_b128 v[178:181], v185 offset:52224
	ds_read_b128 v[204:207], v185 offset:53248
	ds_read_b128 v[208:211], v185 offset:54272
	ds_read_b128 v[214:217], v185 offset:55296
	ds_read_b128 v[218:221], v185 offset:56320
	global_load_lds_dwordx4 v[170:171], off
	s_mov_b32 m0, s85
	v_lshl_add_u64 v[170:171], v[242:243], 0, s[40:41]
	global_load_lds_dwordx4 v[170:171], off
	s_barrier
	s_waitcnt lgkmcnt(0)
	s_setprio 1
	v_mfma_f32_16x16x32_bf16 v[92:95], v[140:143], v[162:165], v[92:95]
	v_mfma_f32_16x16x32_bf16 v[88:91], v[148:151], v[162:165], v[88:91]
	v_mfma_f32_16x16x32_bf16 v[84:87], v[140:143], v[174:177], v[84:87]
	v_mfma_f32_16x16x32_bf16 v[80:83], v[148:151], v[174:177], v[80:83]
	v_mfma_f32_16x16x32_bf16 v[76:79], v[140:143], v[204:207], v[76:79]
	v_mfma_f32_16x16x32_bf16 v[72:75], v[148:151], v[204:207], v[72:75]
	v_mfma_f32_16x16x32_bf16 v[60:63], v[140:143], v[214:217], v[60:63]
	v_mfma_f32_16x16x32_bf16 v[56:59], v[148:151], v[214:217], v[56:59]
	v_mfma_f32_16x16x32_bf16 v[92:95], v[144:147], v[166:169], v[92:95]
	v_mfma_f32_16x16x32_bf16 v[88:91], v[152:155], v[166:169], v[88:91]
	v_mfma_f32_16x16x32_bf16 v[84:87], v[144:147], v[178:181], v[84:87]
	v_mfma_f32_16x16x32_bf16 v[80:83], v[152:155], v[178:181], v[80:83]
	v_mfma_f32_16x16x32_bf16 v[76:79], v[144:147], v[208:211], v[76:79]
	v_mfma_f32_16x16x32_bf16 v[72:75], v[152:155], v[208:211], v[72:75]
	v_mfma_f32_16x16x32_bf16 v[60:63], v[144:147], v[218:221], v[60:63]
	v_mfma_f32_16x16x32_bf16 v[56:59], v[152:155], v[218:221], v[56:59]
	s_setprio 0
	s_barrier
	s_add_u32 s28, s28, 0x40080
	s_addc_u32 s29, s29, 0
	s_mov_b32 m0, s87
	v_lshl_add_u64 v[140:141], s[28:29], 0, v[158:159]
	global_load_lds_dwordx4 v[140:141], off
	s_mov_b32 m0, s44
	v_lshl_add_u64 v[140:141], s[28:29], 0, v[160:161]
	global_load_lds_dwordx4 v[140:141], off
	s_waitcnt vmcnt(6)
	s_barrier
	s_setprio 1
	v_mfma_f32_16x16x32_bf16 v[28:31], v[136:139], v[162:165], v[28:31]
	v_mfma_f32_16x16x32_bf16 v[24:27], v[226:229], v[162:165], v[24:27]
	v_mfma_f32_16x16x32_bf16 v[20:23], v[136:139], v[174:177], v[20:23]
	v_mfma_f32_16x16x32_bf16 v[16:19], v[226:229], v[174:177], v[16:19]
	v_mfma_f32_16x16x32_bf16 v[12:15], v[136:139], v[204:207], v[12:15]
	v_mfma_f32_16x16x32_bf16 v[8:11], v[226:229], v[204:207], v[8:11]
	v_mfma_f32_16x16x32_bf16 v[4:7], v[136:139], v[214:217], v[4:7]
	v_mfma_f32_16x16x32_bf16 v[0:3], v[226:229], v[214:217], v[0:3]
	v_mfma_f32_16x16x32_bf16 v[28:31], v[222:225], v[166:169], v[28:31]
	v_mfma_f32_16x16x32_bf16 v[24:27], v[230:233], v[166:169], v[24:27]
	v_mfma_f32_16x16x32_bf16 v[20:23], v[222:225], v[178:181], v[20:23]
	v_mfma_f32_16x16x32_bf16 v[16:19], v[230:233], v[178:181], v[16:19]
	v_mfma_f32_16x16x32_bf16 v[12:15], v[222:225], v[208:211], v[12:15]
	v_mfma_f32_16x16x32_bf16 v[8:11], v[230:233], v[208:211], v[8:11]
	v_mfma_f32_16x16x32_bf16 v[4:7], v[222:225], v[218:221], v[4:7]
	v_mfma_f32_16x16x32_bf16 v[0:3], v[230:233], v[218:221], v[0:3]
	s_setprio 0
	s_add_i32 vcc_lo, vcc_lo, 2
	s_add_u32 s26, s26, 0x100
	s_addc_u32 s27, s27, 0
	s_add_u32 s9, s9, 0x100
	s_addc_u32 s15, s15, 0
	s_cmp_gt_u32 vcc_lo, 13
	s_barrier
	s_cbranch_scc1 .LBB0_1303

.Lpeel_gu:
	s_mov_b64 s[24:25], 0
	v_mov_b32_e32 v186, v166
	v_mov_b32_e32 v184, v170
	v_mov_b64_e32 v[178:179], v[168:169]
	v_mov_b64_e32 v[176:177], v[174:175]
	ds_read_b128 v[0:3], v191
	ds_read_b128 v[8:11], v191 offset:2048
	ds_read_b128 v[4:7], v193
	ds_read_b128 v[12:15], v193 offset:2048
	s_add_u32 s26, s22, 0x80
	s_addc_u32 s27, s23, 0
	s_and_b64 s[24:25], s[24:25], exec
	s_cselect_b32 s27, s19, s27
	s_cselect_b32 s26, s18, s26
	s_cselect_b32 s25, s17, s3
	s_cselect_b32 s24, s16, s2
	v_lshl_add_u64 v[16:17], s[22:23], 0, v[168:169]
	s_add_i32 m0, s44, 0xc000
	ds_read_b128 v[226:229], v190
	ds_read_b128 v[234:237], v190 offset:2048
	ds_read_b128 v[230:233], v192
	ds_read_b128 v[238:241], v192 offset:2048
	ds_read_b128 v[242:245], v190 offset:4096
	ds_read_b128 v[204:207], v190 offset:6144
	ds_read_b128 v[246:249], v192 offset:4096
	ds_read_b128 v[208:211], v192 offset:6144
	global_load_lds_dwordx4 v[16:17], off
	s_add_i32 m0, s44, 0xe000
	v_lshl_add_u64 v[16:17], s[22:23], 0, v[174:175]
	global_load_lds_dwordx4 v[16:17], off
	s_waitcnt lgkmcnt(8)
	s_barrier
	s_waitcnt lgkmcnt(0)
	s_setprio 1
	v_mfma_scale_f32_16x16x128_f8f6f4 v[156:159], v[0:7], v[226:233], 0, v189, v189 op_sel_hi:[0,0,0]
	v_mfma_scale_f32_16x16x128_f8f6f4 v[148:151], v[8:15], v[226:233], 0, v189, v189 op_sel_hi:[0,0,0]
	v_mfma_scale_f32_16x16x128_f8f6f4 v[140:143], v[0:7], v[234:241], 0, v189, v189 op_sel_hi:[0,0,0]
	v_mfma_scale_f32_16x16x128_f8f6f4 v[132:135], v[8:15], v[234:241], 0, v189, v189 op_sel_hi:[0,0,0]
	v_mfma_scale_f32_16x16x128_f8f6f4 v[124:127], v[0:7], v[242:249], 0, v189, v189 op_sel_hi:[0,0,0]
	v_mfma_scale_f32_16x16x128_f8f6f4 v[116:119], v[8:15], v[242:249], 0, v189, v189 op_sel_hi:[0,0,0]
	v_mfma_scale_f32_16x16x128_f8f6f4 v[108:111], v[0:7], v[204:211], 0, v189, v189 op_sel_hi:[0,0,0]
	v_mfma_scale_f32_16x16x128_f8f6f4 v[100:103], v[8:15], v[204:211], 0, v189, v189 op_sel_hi:[0,0,0]
	s_setprio 0
	s_barrier
	s_mov_b32 m0, s46
	v_lshl_add_u64 v[180:181], s[24:25], 0, v[160:161]
	ds_read_b128 v[16:19], v191 offset:16384
	ds_read_b128 v[24:27], v191 offset:18432
	ds_read_b128 v[20:23], v193 offset:16384
	ds_read_b128 v[28:31], v193 offset:18432
	global_load_lds_dwordx4 v[180:181], off
	s_mov_b32 m0, s47
	v_lshl_add_u64 v[182:183], s[24:25], 0, v[162:163]
	global_load_lds_dwordx4 v[182:183], off
	s_barrier
	s_waitcnt lgkmcnt(0)
	s_setprio 1
	v_mfma_scale_f32_16x16x128_f8f6f4 v[152:155], v[16:23], v[226:233], 0, v189, v189 op_sel_hi:[0,0,0]
	v_mfma_scale_f32_16x16x128_f8f6f4 v[144:147], v[24:31], v[226:233], 0, v189, v189 op_sel_hi:[0,0,0]
	v_mfma_scale_f32_16x16x128_f8f6f4 v[136:139], v[16:23], v[234:241], 0, v189, v189 op_sel_hi:[0,0,0]
	v_mfma_scale_f32_16x16x128_f8f6f4 v[128:131], v[24:31], v[234:241], 0, v189, v189 op_sel_hi:[0,0,0]
	v_mfma_scale_f32_16x16x128_f8f6f4 v[120:123], v[16:23], v[242:249], 0, v189, v189 op_sel_hi:[0,0,0]
	v_mfma_scale_f32_16x16x128_f8f6f4 v[112:115], v[24:31], v[242:249], 0, v189, v189 op_sel_hi:[0,0,0]
	v_mfma_scale_f32_16x16x128_f8f6f4 v[104:107], v[16:23], v[204:211], 0, v189, v189 op_sel_hi:[0,0,0]
	v_mfma_scale_f32_16x16x128_f8f6f4 v[96:99], v[24:31], v[204:211], 0, v189, v189 op_sel_hi:[0,0,0]
	s_setprio 0
	s_mov_b32 m0, s44
	s_barrier
	ds_read_b128 v[204:207], v190 offset:16384
	ds_read_b128 v[226:229], v190 offset:18432
	ds_read_b128 v[208:211], v192 offset:16384
	ds_read_b128 v[230:233], v192 offset:18432
	ds_read_b128 v[234:237], v190 offset:20480
	ds_read_b128 v[242:245], v190 offset:22528
	ds_read_b128 v[238:241], v192 offset:20480
	ds_read_b128 v[246:249], v192 offset:22528
	global_load_lds_dwordx4 v186, s[26:27]
	s_mov_b32 m0, s50
	v_mov_b32_e32 v187, v173
	global_load_lds_dwordx4 v184, s[26:27]
	s_barrier
	s_waitcnt lgkmcnt(0)
	v_mov_b32_e32 v185, v173
	v_lshl_add_u64 v[186:187], s[26:27], 0, v[186:187]
	v_lshl_add_u64 v[184:185], s[26:27], 0, v[184:185]
	s_setprio 1
	s_waitcnt lgkmcnt(0)
	v_mfma_scale_f32_16x16x128_f8f6f4 v[92:95], v[0:7], v[204:211], 0, v189, v189 op_sel_hi:[0,0,0]
	v_mfma_scale_f32_16x16x128_f8f6f4 v[84:87], v[8:15], v[204:211], 0, v189, v189 op_sel_hi:[0,0,0]
	v_mfma_scale_f32_16x16x128_f8f6f4 v[76:79], v[0:7], v[226:233], 0, v189, v189 op_sel_hi:[0,0,0]
	v_mfma_scale_f32_16x16x128_f8f6f4 v[68:71], v[8:15], v[226:233], 0, v189, v189 op_sel_hi:[0,0,0]
	v_mfma_scale_f32_16x16x128_f8f6f4 v[60:63], v[0:7], v[234:241], 0, v189, v189 op_sel_hi:[0,0,0]
	v_mfma_scale_f32_16x16x128_f8f6f4 v[52:55], v[8:15], v[234:241], 0, v189, v189 op_sel_hi:[0,0,0]
	v_mfma_scale_f32_16x16x128_f8f6f4 v[44:47], v[0:7], v[242:249], 0, v189, v189 op_sel_hi:[0,0,0]
	v_mfma_scale_f32_16x16x128_f8f6f4 v[36:39], v[8:15], v[242:249], 0, v189, v189 op_sel_hi:[0,0,0]
	s_setprio 0
	s_barrier
	s_add_u32 s72, s24, 0x20000
	s_addc_u32 s73, s25, 0
	s_mov_b32 m0, s51
	v_lshl_add_u64 v[0:1], s[72:73], 0, v[160:161]
	global_load_lds_dwordx4 v[0:1], off
	s_mov_b32 m0, s56
	v_lshl_add_u64 v[0:1], s[72:73], 0, v[162:163]
	global_load_lds_dwordx4 v[0:1], off
	s_waitcnt vmcnt(6)
	s_barrier
	s_setprio 1
	v_mfma_scale_f32_16x16x128_f8f6f4 v[88:91], v[16:23], v[204:211], 0, v189, v189 op_sel_hi:[0,0,0]
	v_mfma_scale_f32_16x16x128_f8f6f4 v[80:83], v[24:31], v[204:211], 0, v189, v189 op_sel_hi:[0,0,0]
	v_mfma_scale_f32_16x16x128_f8f6f4 v[72:75], v[16:23], v[226:233], 0, v189, v189 op_sel_hi:[0,0,0]
	v_mfma_scale_f32_16x16x128_f8f6f4 v[64:67], v[24:31], v[226:233], 0, v189, v189 op_sel_hi:[0,0,0]
	v_mfma_scale_f32_16x16x128_f8f6f4 v[56:59], v[16:23], v[234:241], 0, v189, v189 op_sel_hi:[0,0,0]
	v_mfma_scale_f32_16x16x128_f8f6f4 v[48:51], v[24:31], v[234:241], 0, v189, v189 op_sel_hi:[0,0,0]
	v_mfma_scale_f32_16x16x128_f8f6f4 v[40:43], v[16:23], v[242:249], 0, v189, v189 op_sel_hi:[0,0,0]
	v_mfma_scale_f32_16x16x128_f8f6f4 v[32:35], v[24:31], v[242:249], 0, v189, v189 op_sel_hi:[0,0,0]
	s_setprio 0
	s_barrier
	ds_read_b128 v[0:3], v191 offset:32768
	ds_read_b128 v[8:11], v191 offset:34816
	ds_read_b128 v[4:7], v193 offset:32768
	ds_read_b128 v[12:15], v193 offset:34816
	s_mov_b32 m0, s65
	v_lshl_add_u64 v[178:179], s[26:27], 0, v[178:179]
	ds_read_b128 v[16:19], v190 offset:32768
	ds_read_b128 v[24:27], v190 offset:34816
	ds_read_b128 v[20:23], v192 offset:32768
	ds_read_b128 v[28:31], v192 offset:34816
	ds_read_b128 v[204:207], v190 offset:36864
	ds_read_b128 v[226:229], v190 offset:38912
	ds_read_b128 v[208:211], v192 offset:36864
	ds_read_b128 v[230:233], v192 offset:38912
	global_load_lds_dwordx4 v[178:179], off
	s_mov_b32 m0, s70
	v_lshl_add_u64 v[176:177], s[26:27], 0, v[176:177]
	global_load_lds_dwordx4 v[176:177], off
	s_waitcnt lgkmcnt(8)
	s_barrier
	s_waitcnt lgkmcnt(0)
	s_setprio 1
	v_mfma_scale_f32_16x16x128_f8f6f4 v[156:159], v[0:7], v[16:23], v[156:159], v189, v189 op_sel_hi:[0,0,0]
	v_mfma_scale_f32_16x16x128_f8f6f4 v[148:151], v[8:15], v[16:23], v[148:151], v189, v189 op_sel_hi:[0,0,0]
	v_mfma_scale_f32_16x16x128_f8f6f4 v[140:143], v[0:7], v[24:31], v[140:143], v189, v189 op_sel_hi:[0,0,0]
	v_mfma_scale_f32_16x16x128_f8f6f4 v[132:135], v[8:15], v[24:31], v[132:135], v189, v189 op_sel_hi:[0,0,0]
	v_mfma_scale_f32_16x16x128_f8f6f4 v[124:127], v[0:7], v[204:211], v[124:127], v189, v189 op_sel_hi:[0,0,0]
	v_mfma_scale_f32_16x16x128_f8f6f4 v[116:119], v[8:15], v[204:211], v[116:119], v189, v189 op_sel_hi:[0,0,0]
	v_mfma_scale_f32_16x16x128_f8f6f4 v[108:111], v[0:7], v[226:233], v[108:111], v189, v189 op_sel_hi:[0,0,0]
	v_mfma_scale_f32_16x16x128_f8f6f4 v[100:103], v[8:15], v[226:233], v[100:103], v189, v189 op_sel_hi:[0,0,0]
	s_setprio 0
	s_barrier
	s_mov_b32 m0, s71
	v_lshl_add_u64 v[176:177], v[180:181], 0, s[40:41]
	ds_read_b128 v[234:237], v191 offset:49152
	ds_read_b128 v[242:245], v191 offset:51200
	ds_read_b128 v[238:241], v193 offset:49152
	ds_read_b128 v[246:249], v193 offset:51200
	global_load_lds_dwordx4 v[176:177], off
	s_mov_b32 m0, s80
	v_lshl_add_u64 v[176:177], v[182:183], 0, s[40:41]
	global_load_lds_dwordx4 v[176:177], off
	s_barrier
	s_waitcnt lgkmcnt(0)
	s_setprio 1
	v_mfma_scale_f32_16x16x128_f8f6f4 v[152:155], v[234:241], v[16:23], v[152:155], v189, v189 op_sel_hi:[0,0,0]
	v_mfma_scale_f32_16x16x128_f8f6f4 v[144:147], v[242:249], v[16:23], v[144:147], v189, v189 op_sel_hi:[0,0,0]
	v_mfma_scale_f32_16x16x128_f8f6f4 v[136:139], v[234:241], v[24:31], v[136:139], v189, v189 op_sel_hi:[0,0,0]
	v_mfma_scale_f32_16x16x128_f8f6f4 v[128:131], v[242:249], v[24:31], v[128:131], v189, v189 op_sel_hi:[0,0,0]
	v_mfma_scale_f32_16x16x128_f8f6f4 v[120:123], v[234:241], v[204:211], v[120:123], v189, v189 op_sel_hi:[0,0,0]
	v_mfma_scale_f32_16x16x128_f8f6f4 v[112:115], v[242:249], v[204:211], v[112:115], v189, v189 op_sel_hi:[0,0,0]
	v_mfma_scale_f32_16x16x128_f8f6f4 v[104:107], v[234:241], v[226:233], v[104:107], v189, v189 op_sel_hi:[0,0,0]
	v_mfma_scale_f32_16x16x128_f8f6f4 v[96:99], v[242:249], v[226:233], v[96:99], v189, v189 op_sel_hi:[0,0,0]
	s_setprio 0
	s_mov_b32 m0, s81
	v_lshl_add_u64 v[186:187], v[186:187], 0, s[40:41]
	s_barrier
	ds_read_b128 v[16:19], v190 offset:49152
	ds_read_b128 v[24:27], v190 offset:51200
	ds_read_b128 v[20:23], v192 offset:49152
	ds_read_b128 v[28:31], v192 offset:51200
	ds_read_b128 v[176:179], v190 offset:53248
	ds_read_b128 v[204:207], v190 offset:55296
	ds_read_b128 v[180:183], v192 offset:53248
	ds_read_b128 v[208:211], v192 offset:55296
	global_load_lds_dwordx4 v[186:187], off
	s_mov_b32 m0, s82
	v_lshl_add_u64 v[184:185], v[184:185], 0, s[40:41]
	global_load_lds_dwordx4 v[184:185], off
	s_barrier
	s_waitcnt lgkmcnt(0)
	s_setprio 1
	v_mfma_scale_f32_16x16x128_f8f6f4 v[92:95], v[0:7], v[16:23], v[92:95], v189, v189 op_sel_hi:[0,0,0]
	v_mfma_scale_f32_16x16x128_f8f6f4 v[84:87], v[8:15], v[16:23], v[84:87], v189, v189 op_sel_hi:[0,0,0]
	v_mfma_scale_f32_16x16x128_f8f6f4 v[76:79], v[0:7], v[24:31], v[76:79], v189, v189 op_sel_hi:[0,0,0]
	v_mfma_scale_f32_16x16x128_f8f6f4 v[68:71], v[8:15], v[24:31], v[68:71], v189, v189 op_sel_hi:[0,0,0]
	v_mfma_scale_f32_16x16x128_f8f6f4 v[60:63], v[0:7], v[176:183], v[60:63], v189, v189 op_sel_hi:[0,0,0]
	v_mfma_scale_f32_16x16x128_f8f6f4 v[52:55], v[8:15], v[176:183], v[52:55], v189, v189 op_sel_hi:[0,0,0]
	v_mfma_scale_f32_16x16x128_f8f6f4 v[44:47], v[0:7], v[204:211], v[44:47], v189, v189 op_sel_hi:[0,0,0]
	v_mfma_scale_f32_16x16x128_f8f6f4 v[36:39], v[8:15], v[204:211], v[36:39], v189, v189 op_sel_hi:[0,0,0]
	s_setprio 0
	s_barrier
	s_add_u32 s24, s24, 0x20080
	s_addc_u32 s25, s25, 0
	s_mov_b32 m0, s83
	v_lshl_add_u64 v[0:1], s[24:25], 0, v[160:161]
	global_load_lds_dwordx4 v[0:1], off
	s_mov_b32 m0, s85
	v_lshl_add_u64 v[0:1], s[24:25], 0, v[162:163]
	global_load_lds_dwordx4 v[0:1], off
	s_waitcnt vmcnt(6)
	s_barrier
	s_setprio 1
	v_mfma_scale_f32_16x16x128_f8f6f4 v[88:91], v[234:241], v[16:23], v[88:91], v189, v189 op_sel_hi:[0,0,0]
	v_mfma_scale_f32_16x16x128_f8f6f4 v[80:83], v[242:249], v[16:23], v[80:83], v189, v189 op_sel_hi:[0,0,0]
	v_mfma_scale_f32_16x16x128_f8f6f4 v[72:75], v[234:241], v[24:31], v[72:75], v189, v189 op_sel_hi:[0,0,0]
	v_mfma_scale_f32_16x16x128_f8f6f4 v[64:67], v[242:249], v[24:31], v[64:67], v189, v189 op_sel_hi:[0,0,0]
	v_mfma_scale_f32_16x16x128_f8f6f4 v[56:59], v[234:241], v[176:183], v[56:59], v189, v189 op_sel_hi:[0,0,0]
	v_mfma_scale_f32_16x16x128_f8f6f4 v[48:51], v[242:249], v[176:183], v[48:51], v189, v189 op_sel_hi:[0,0,0]
	v_mfma_scale_f32_16x16x128_f8f6f4 v[40:43], v[234:241], v[204:211], v[40:43], v189, v189 op_sel_hi:[0,0,0]
	v_mfma_scale_f32_16x16x128_f8f6f4 v[32:35], v[242:249], v[204:211], v[32:35], v189, v189 op_sel_hi:[0,0,0]
	s_setprio 0
	s_add_i32 s64, s64, 2
	s_add_u32 s22, s22, 0x100
	s_addc_u32 s23, s23, 0
	s_add_u32 s2, s2, 0x100
	s_addc_u32 s3, s3, 0
	s_cmp_gt_u32 s64, 5
	s_barrier
	s_branch .LBB0_1556

.LBB0_1555:
	ds_read_b128 v[0:3], v191
	ds_read_b128 v[8:11], v191 offset:2048
	ds_read_b128 v[4:7], v193
	ds_read_b128 v[12:15], v193 offset:2048
	s_add_u32 s26, s22, 0x80
	s_addc_u32 s27, s23, 0
	s_and_b64 s[24:25], s[24:25], exec
	s_cselect_b32 s27, s19, s27
	s_cselect_b32 s26, s18, s26
	s_cselect_b32 s25, s17, s3
	s_cselect_b32 s24, s16, s2
	v_lshl_add_u64 v[16:17], s[22:23], 0, v[168:169]
	s_add_i32 m0, s44, 0xc000
	ds_read_b128 v[226:229], v190
	ds_read_b128 v[234:237], v190 offset:2048
	ds_read_b128 v[230:233], v192
	ds_read_b128 v[238:241], v192 offset:2048
	ds_read_b128 v[242:245], v190 offset:4096
	ds_read_b128 v[204:207], v190 offset:6144
	ds_read_b128 v[246:249], v192 offset:4096
	ds_read_b128 v[208:211], v192 offset:6144
	global_load_lds_dwordx4 v[16:17], off
	s_add_i32 m0, s44, 0xe000
	v_lshl_add_u64 v[16:17], s[22:23], 0, v[174:175]
	global_load_lds_dwordx4 v[16:17], off
	s_waitcnt lgkmcnt(8)
	s_barrier
	s_waitcnt lgkmcnt(0)
	s_setprio 1
	v_mfma_scale_f32_16x16x128_f8f6f4 v[156:159], v[0:7], v[226:233], v[156:159], v189, v189 op_sel_hi:[0,0,0]
	v_mfma_scale_f32_16x16x128_f8f6f4 v[148:151], v[8:15], v[226:233], v[148:151], v189, v189 op_sel_hi:[0,0,0]
	v_mfma_scale_f32_16x16x128_f8f6f4 v[140:143], v[0:7], v[234:241], v[140:143], v189, v189 op_sel_hi:[0,0,0]
	v_mfma_scale_f32_16x16x128_f8f6f4 v[132:135], v[8:15], v[234:241], v[132:135], v189, v189 op_sel_hi:[0,0,0]
	v_mfma_scale_f32_16x16x128_f8f6f4 v[124:127], v[0:7], v[242:249], v[124:127], v189, v189 op_sel_hi:[0,0,0]
	v_mfma_scale_f32_16x16x128_f8f6f4 v[116:119], v[8:15], v[242:249], v[116:119], v189, v189 op_sel_hi:[0,0,0]
	v_mfma_scale_f32_16x16x128_f8f6f4 v[108:111], v[0:7], v[204:211], v[108:111], v189, v189 op_sel_hi:[0,0,0]
	v_mfma_scale_f32_16x16x128_f8f6f4 v[100:103], v[8:15], v[204:211], v[100:103], v189, v189 op_sel_hi:[0,0,0]
	s_setprio 0
	s_barrier
	s_mov_b32 m0, s46
	v_lshl_add_u64 v[180:181], s[24:25], 0, v[160:161]
	ds_read_b128 v[16:19], v191 offset:16384
	ds_read_b128 v[24:27], v191 offset:18432
	ds_read_b128 v[20:23], v193 offset:16384
	ds_read_b128 v[28:31], v193 offset:18432
	global_load_lds_dwordx4 v[180:181], off
	s_mov_b32 m0, s47
	v_lshl_add_u64 v[182:183], s[24:25], 0, v[162:163]
	global_load_lds_dwordx4 v[182:183], off
	s_barrier
	s_waitcnt lgkmcnt(0)
	s_setprio 1
	v_mfma_scale_f32_16x16x128_f8f6f4 v[152:155], v[16:23], v[226:233], v[152:155], v189, v189 op_sel_hi:[0,0,0]
	v_mfma_scale_f32_16x16x128_f8f6f4 v[144:147], v[24:31], v[226:233], v[144:147], v189, v189 op_sel_hi:[0,0,0]
	v_mfma_scale_f32_16x16x128_f8f6f4 v[136:139], v[16:23], v[234:241], v[136:139], v189, v189 op_sel_hi:[0,0,0]
	v_mfma_scale_f32_16x16x128_f8f6f4 v[128:131], v[24:31], v[234:241], v[128:131], v189, v189 op_sel_hi:[0,0,0]
	v_mfma_scale_f32_16x16x128_f8f6f4 v[120:123], v[16:23], v[242:249], v[120:123], v189, v189 op_sel_hi:[0,0,0]
	v_mfma_scale_f32_16x16x128_f8f6f4 v[112:115], v[24:31], v[242:249], v[112:115], v189, v189 op_sel_hi:[0,0,0]
	v_mfma_scale_f32_16x16x128_f8f6f4 v[104:107], v[16:23], v[204:211], v[104:107], v189, v189 op_sel_hi:[0,0,0]
	v_mfma_scale_f32_16x16x128_f8f6f4 v[96:99], v[24:31], v[204:211], v[96:99], v189, v189 op_sel_hi:[0,0,0]
	s_setprio 0
	s_mov_b32 m0, s44
	s_barrier
	ds_read_b128 v[204:207], v190 offset:16384
	ds_read_b128 v[226:229], v190 offset:18432
	ds_read_b128 v[208:211], v192 offset:16384
	ds_read_b128 v[230:233], v192 offset:18432
	ds_read_b128 v[234:237], v190 offset:20480
	ds_read_b128 v[242:245], v190 offset:22528
	ds_read_b128 v[238:241], v192 offset:20480
	ds_read_b128 v[246:249], v192 offset:22528
	global_load_lds_dwordx4 v186, s[26:27]
	s_mov_b32 m0, s50
	v_mov_b32_e32 v187, v173
	global_load_lds_dwordx4 v184, s[26:27]
	s_barrier
	s_waitcnt lgkmcnt(0)
	v_mov_b32_e32 v185, v173
	v_lshl_add_u64 v[186:187], s[26:27], 0, v[186:187]
	v_lshl_add_u64 v[184:185], s[26:27], 0, v[184:185]
	s_setprio 1
	s_waitcnt lgkmcnt(0)
	v_mfma_scale_f32_16x16x128_f8f6f4 v[92:95], v[0:7], v[204:211], v[92:95], v189, v189 op_sel_hi:[0,0,0]
	v_mfma_scale_f32_16x16x128_f8f6f4 v[84:87], v[8:15], v[204:211], v[84:87], v189, v189 op_sel_hi:[0,0,0]
	v_mfma_scale_f32_16x16x128_f8f6f4 v[76:79], v[0:7], v[226:233], v[76:79], v189, v189 op_sel_hi:[0,0,0]
	v_mfma_scale_f32_16x16x128_f8f6f4 v[68:71], v[8:15], v[226:233], v[68:71], v189, v189 op_sel_hi:[0,0,0]
	v_mfma_scale_f32_16x16x128_f8f6f4 v[60:63], v[0:7], v[234:241], v[60:63], v189, v189 op_sel_hi:[0,0,0]
	v_mfma_scale_f32_16x16x128_f8f6f4 v[52:55], v[8:15], v[234:241], v[52:55], v189, v189 op_sel_hi:[0,0,0]
	v_mfma_scale_f32_16x16x128_f8f6f4 v[44:47], v[0:7], v[242:249], v[44:47], v189, v189 op_sel_hi:[0,0,0]
	v_mfma_scale_f32_16x16x128_f8f6f4 v[36:39], v[8:15], v[242:249], v[36:39], v189, v189 op_sel_hi:[0,0,0]
	s_setprio 0
	s_barrier
	s_add_u32 s72, s24, 0x20000
	s_addc_u32 s73, s25, 0
	s_mov_b32 m0, s51
	v_lshl_add_u64 v[0:1], s[72:73], 0, v[160:161]
	global_load_lds_dwordx4 v[0:1], off
	s_mov_b32 m0, s56
	v_lshl_add_u64 v[0:1], s[72:73], 0, v[162:163]
	global_load_lds_dwordx4 v[0:1], off
	s_waitcnt vmcnt(6)
	s_barrier
	s_setprio 1
	v_mfma_scale_f32_16x16x128_f8f6f4 v[88:91], v[16:23], v[204:211], v[88:91], v189, v189 op_sel_hi:[0,0,0]
	v_mfma_scale_f32_16x16x128_f8f6f4 v[80:83], v[24:31], v[204:211], v[80:83], v189, v189 op_sel_hi:[0,0,0]
	v_mfma_scale_f32_16x16x128_f8f6f4 v[72:75], v[16:23], v[226:233], v[72:75], v189, v189 op_sel_hi:[0,0,0]
	v_mfma_scale_f32_16x16x128_f8f6f4 v[64:67], v[24:31], v[226:233], v[64:67], v189, v189 op_sel_hi:[0,0,0]
	v_mfma_scale_f32_16x16x128_f8f6f4 v[56:59], v[16:23], v[234:241], v[56:59], v189, v189 op_sel_hi:[0,0,0]
	v_mfma_scale_f32_16x16x128_f8f6f4 v[48:51], v[24:31], v[234:241], v[48:51], v189, v189 op_sel_hi:[0,0,0]
	v_mfma_scale_f32_16x16x128_f8f6f4 v[40:43], v[16:23], v[242:249], v[40:43], v189, v189 op_sel_hi:[0,0,0]
	v_mfma_scale_f32_16x16x128_f8f6f4 v[32:35], v[24:31], v[242:249], v[32:35], v189, v189 op_sel_hi:[0,0,0]
	s_setprio 0
	s_barrier
	ds_read_b128 v[0:3], v191 offset:32768
	ds_read_b128 v[8:11], v191 offset:34816
	ds_read_b128 v[4:7], v193 offset:32768
	ds_read_b128 v[12:15], v193 offset:34816
	s_mov_b32 m0, s65
	v_lshl_add_u64 v[178:179], s[26:27], 0, v[178:179]
	ds_read_b128 v[16:19], v190 offset:32768
	ds_read_b128 v[24:27], v190 offset:34816
	ds_read_b128 v[20:23], v192 offset:32768
	ds_read_b128 v[28:31], v192 offset:34816
	ds_read_b128 v[204:207], v190 offset:36864
	ds_read_b128 v[226:229], v190 offset:38912
	ds_read_b128 v[208:211], v192 offset:36864
	ds_read_b128 v[230:233], v192 offset:38912
	global_load_lds_dwordx4 v[178:179], off
	s_mov_b32 m0, s70
	v_lshl_add_u64 v[176:177], s[26:27], 0, v[176:177]
	global_load_lds_dwordx4 v[176:177], off
	s_waitcnt lgkmcnt(8)
	s_barrier
	s_waitcnt lgkmcnt(0)
	s_setprio 1
	v_mfma_scale_f32_16x16x128_f8f6f4 v[156:159], v[0:7], v[16:23], v[156:159], v189, v189 op_sel_hi:[0,0,0]
	v_mfma_scale_f32_16x16x128_f8f6f4 v[148:151], v[8:15], v[16:23], v[148:151], v189, v189 op_sel_hi:[0,0,0]
	v_mfma_scale_f32_16x16x128_f8f6f4 v[140:143], v[0:7], v[24:31], v[140:143], v189, v189 op_sel_hi:[0,0,0]
	v_mfma_scale_f32_16x16x128_f8f6f4 v[132:135], v[8:15], v[24:31], v[132:135], v189, v189 op_sel_hi:[0,0,0]
	v_mfma_scale_f32_16x16x128_f8f6f4 v[124:127], v[0:7], v[204:211], v[124:127], v189, v189 op_sel_hi:[0,0,0]
	v_mfma_scale_f32_16x16x128_f8f6f4 v[116:119], v[8:15], v[204:211], v[116:119], v189, v189 op_sel_hi:[0,0,0]
	v_mfma_scale_f32_16x16x128_f8f6f4 v[108:111], v[0:7], v[226:233], v[108:111], v189, v189 op_sel_hi:[0,0,0]
	v_mfma_scale_f32_16x16x128_f8f6f4 v[100:103], v[8:15], v[226:233], v[100:103], v189, v189 op_sel_hi:[0,0,0]
	s_setprio 0
	s_barrier
	s_mov_b32 m0, s71
	v_lshl_add_u64 v[176:177], v[180:181], 0, s[40:41]
	ds_read_b128 v[234:237], v191 offset:49152
	ds_read_b128 v[242:245], v191 offset:51200
	ds_read_b128 v[238:241], v193 offset:49152
	ds_read_b128 v[246:249], v193 offset:51200
	global_load_lds_dwordx4 v[176:177], off
	s_mov_b32 m0, s80
	v_lshl_add_u64 v[176:177], v[182:183], 0, s[40:41]
	global_load_lds_dwordx4 v[176:177], off
	s_barrier
	s_waitcnt lgkmcnt(0)
	s_setprio 1
	v_mfma_scale_f32_16x16x128_f8f6f4 v[152:155], v[234:241], v[16:23], v[152:155], v189, v189 op_sel_hi:[0,0,0]
	v_mfma_scale_f32_16x16x128_f8f6f4 v[144:147], v[242:249], v[16:23], v[144:147], v189, v189 op_sel_hi:[0,0,0]
	v_mfma_scale_f32_16x16x128_f8f6f4 v[136:139], v[234:241], v[24:31], v[136:139], v189, v189 op_sel_hi:[0,0,0]
	v_mfma_scale_f32_16x16x128_f8f6f4 v[128:131], v[242:249], v[24:31], v[128:131], v189, v189 op_sel_hi:[0,0,0]
	v_mfma_scale_f32_16x16x128_f8f6f4 v[120:123], v[234:241], v[204:211], v[120:123], v189, v189 op_sel_hi:[0,0,0]
	v_mfma_scale_f32_16x16x128_f8f6f4 v[112:115], v[242:249], v[204:211], v[112:115], v189, v189 op_sel_hi:[0,0,0]
	v_mfma_scale_f32_16x16x128_f8f6f4 v[104:107], v[234:241], v[226:233], v[104:107], v189, v189 op_sel_hi:[0,0,0]
	v_mfma_scale_f32_16x16x128_f8f6f4 v[96:99], v[242:249], v[226:233], v[96:99], v189, v189 op_sel_hi:[0,0,0]
	s_setprio 0
	s_mov_b32 m0, s81
	v_lshl_add_u64 v[186:187], v[186:187], 0, s[40:41]
	s_barrier
	ds_read_b128 v[16:19], v190 offset:49152
	ds_read_b128 v[24:27], v190 offset:51200
	ds_read_b128 v[20:23], v192 offset:49152
	ds_read_b128 v[28:31], v192 offset:51200
	ds_read_b128 v[176:179], v190 offset:53248
	ds_read_b128 v[204:207], v190 offset:55296
	ds_read_b128 v[180:183], v192 offset:53248
	ds_read_b128 v[208:211], v192 offset:55296
	global_load_lds_dwordx4 v[186:187], off
	s_mov_b32 m0, s82
	v_lshl_add_u64 v[184:185], v[184:185], 0, s[40:41]
	global_load_lds_dwordx4 v[184:185], off
	s_barrier
	s_waitcnt lgkmcnt(0)
	s_setprio 1
	v_mfma_scale_f32_16x16x128_f8f6f4 v[92:95], v[0:7], v[16:23], v[92:95], v189, v189 op_sel_hi:[0,0,0]
	v_mfma_scale_f32_16x16x128_f8f6f4 v[84:87], v[8:15], v[16:23], v[84:87], v189, v189 op_sel_hi:[0,0,0]
	v_mfma_scale_f32_16x16x128_f8f6f4 v[76:79], v[0:7], v[24:31], v[76:79], v189, v189 op_sel_hi:[0,0,0]
	v_mfma_scale_f32_16x16x128_f8f6f4 v[68:71], v[8:15], v[24:31], v[68:71], v189, v189 op_sel_hi:[0,0,0]
	v_mfma_scale_f32_16x16x128_f8f6f4 v[60:63], v[0:7], v[176:183], v[60:63], v189, v189 op_sel_hi:[0,0,0]
	v_mfma_scale_f32_16x16x128_f8f6f4 v[52:55], v[8:15], v[176:183], v[52:55], v189, v189 op_sel_hi:[0,0,0]
	v_mfma_scale_f32_16x16x128_f8f6f4 v[44:47], v[0:7], v[204:211], v[44:47], v189, v189 op_sel_hi:[0,0,0]
	v_mfma_scale_f32_16x16x128_f8f6f4 v[36:39], v[8:15], v[204:211], v[36:39], v189, v189 op_sel_hi:[0,0,0]
	s_setprio 0
	s_barrier
	s_add_u32 s24, s24, 0x20080
	s_addc_u32 s25, s25, 0
	s_mov_b32 m0, s83
	v_lshl_add_u64 v[0:1], s[24:25], 0, v[160:161]
	global_load_lds_dwordx4 v[0:1], off
	s_mov_b32 m0, s85
	v_lshl_add_u64 v[0:1], s[24:25], 0, v[162:163]
	global_load_lds_dwordx4 v[0:1], off
	s_waitcnt vmcnt(6)
	s_barrier
	s_setprio 1
	v_mfma_scale_f32_16x16x128_f8f6f4 v[88:91], v[234:241], v[16:23], v[88:91], v189, v189 op_sel_hi:[0,0,0]
	v_mfma_scale_f32_16x16x128_f8f6f4 v[80:83], v[242:249], v[16:23], v[80:83], v189, v189 op_sel_hi:[0,0,0]
	v_mfma_scale_f32_16x16x128_f8f6f4 v[72:75], v[234:241], v[24:31], v[72:75], v189, v189 op_sel_hi:[0,0,0]
	v_mfma_scale_f32_16x16x128_f8f6f4 v[64:67], v[242:249], v[24:31], v[64:67], v189, v189 op_sel_hi:[0,0,0]
	v_mfma_scale_f32_16x16x128_f8f6f4 v[56:59], v[234:241], v[176:183], v[56:59], v189, v189 op_sel_hi:[0,0,0]
	v_mfma_scale_f32_16x16x128_f8f6f4 v[48:51], v[242:249], v[176:183], v[48:51], v189, v189 op_sel_hi:[0,0,0]
	v_mfma_scale_f32_16x16x128_f8f6f4 v[40:43], v[234:241], v[204:211], v[40:43], v189, v189 op_sel_hi:[0,0,0]
	v_mfma_scale_f32_16x16x128_f8f6f4 v[32:35], v[242:249], v[204:211], v[32:35], v189, v189 op_sel_hi:[0,0,0]
	s_setprio 0
	s_add_i32 s64, s64, 2
	s_add_u32 s22, s22, 0x100
	s_addc_u32 s23, s23, 0
	s_add_u32 s2, s2, 0x100
	s_addc_u32 s3, s3, 0
	s_cmp_gt_u32 s64, 5
	s_barrier
	s_cbranch_scc1 .LBB0_1540

.Lpeel_dn:
	s_mov_b64 s[24:25], 0
	v_mov_b64_e32 v[176:177], v[170:171]
	v_mov_b64_e32 v[178:179], v[166:167]
	v_mov_b32_e32 v184, v174
	v_mov_b32_e32 v172, v168
	ds_read_b128 v[0:3], v190
	ds_read_b128 v[8:11], v190 offset:2048
	ds_read_b128 v[4:7], v192
	ds_read_b128 v[12:15], v192 offset:2048
	s_add_u32 s26, s22, 0x80
	s_addc_u32 s27, s23, 0
	s_and_b64 s[24:25], s[24:25], exec
	s_cselect_b32 s27, s19, s27
	s_cselect_b32 s26, s18, s26
	s_cselect_b32 s25, s17, s83
	s_cselect_b32 s24, s16, s7
	v_lshl_add_u64 v[16:17], s[22:23], 0, v[166:167]
	s_add_i32 m0, s13, 0xc000
	ds_read_b128 v[204:207], v189
	ds_read_b128 v[216:219], v189 offset:2048
	ds_read_b128 v[208:211], v191
	ds_read_b128 v[220:223], v191 offset:2048
	ds_read_b128 v[224:227], v189 offset:4096
	ds_read_b128 v[232:235], v189 offset:6144
	ds_read_b128 v[228:231], v191 offset:4096
	ds_read_b128 v[236:239], v191 offset:6144
	global_load_lds_dwordx4 v[16:17], off
	s_add_i32 m0, s13, 0xe000
	v_lshl_add_u64 v[16:17], s[22:23], 0, v[170:171]
	global_load_lds_dwordx4 v[16:17], off
	s_waitcnt lgkmcnt(8)
	s_barrier
	s_waitcnt lgkmcnt(0)
	s_setprio 1
	v_mfma_scale_f32_16x16x128_f8f6f4 v[156:159], v[0:7], v[204:211], 0, v188, v188 op_sel_hi:[0,0,0]
	v_mfma_scale_f32_16x16x128_f8f6f4 v[152:155], v[8:15], v[204:211], 0, v188, v188 op_sel_hi:[0,0,0]
	v_mfma_scale_f32_16x16x128_f8f6f4 v[148:151], v[0:7], v[216:223], 0, v188, v188 op_sel_hi:[0,0,0]
	v_mfma_scale_f32_16x16x128_f8f6f4 v[144:147], v[8:15], v[216:223], 0, v188, v188 op_sel_hi:[0,0,0]
	v_mfma_scale_f32_16x16x128_f8f6f4 v[140:143], v[0:7], v[224:231], 0, v188, v188 op_sel_hi:[0,0,0]
	v_mfma_scale_f32_16x16x128_f8f6f4 v[136:139], v[8:15], v[224:231], 0, v188, v188 op_sel_hi:[0,0,0]
	v_mfma_scale_f32_16x16x128_f8f6f4 v[132:135], v[0:7], v[232:239], 0, v188, v188 op_sel_hi:[0,0,0]
	v_mfma_scale_f32_16x16x128_f8f6f4 v[128:131], v[8:15], v[232:239], 0, v188, v188 op_sel_hi:[0,0,0]
	s_setprio 0
	s_barrier
	s_mov_b32 m0, s15
	v_lshl_add_u64 v[180:181], s[24:25], 0, v[162:163]
	ds_read_b128 v[16:19], v190 offset:16384
	ds_read_b128 v[24:27], v190 offset:18432
	ds_read_b128 v[20:23], v192 offset:16384
	ds_read_b128 v[28:31], v192 offset:18432
	global_load_lds_dwordx4 v[180:181], off
	s_mov_b32 m0, s31
	v_lshl_add_u64 v[182:183], s[24:25], 0, v[164:165]
	global_load_lds_dwordx4 v[182:183], off
	s_barrier
	s_waitcnt lgkmcnt(0)
	s_setprio 1
	v_mfma_scale_f32_16x16x128_f8f6f4 v[100:103], v[16:23], v[204:211], 0, v188, v188 op_sel_hi:[0,0,0]
	v_mfma_scale_f32_16x16x128_f8f6f4 v[96:99], v[24:31], v[204:211], 0, v188, v188 op_sel_hi:[0,0,0]
	v_mfma_scale_f32_16x16x128_f8f6f4 v[84:87], v[16:23], v[216:223], 0, v188, v188 op_sel_hi:[0,0,0]
	v_mfma_scale_f32_16x16x128_f8f6f4 v[80:83], v[24:31], v[216:223], 0, v188, v188 op_sel_hi:[0,0,0]
	v_mfma_scale_f32_16x16x128_f8f6f4 v[76:79], v[16:23], v[224:231], 0, v188, v188 op_sel_hi:[0,0,0]
	v_mfma_scale_f32_16x16x128_f8f6f4 v[72:75], v[24:31], v[224:231], 0, v188, v188 op_sel_hi:[0,0,0]
	v_mfma_scale_f32_16x16x128_f8f6f4 v[68:71], v[16:23], v[232:239], 0, v188, v188 op_sel_hi:[0,0,0]
	v_mfma_scale_f32_16x16x128_f8f6f4 v[64:67], v[24:31], v[232:239], 0, v188, v188 op_sel_hi:[0,0,0]
	s_setprio 0
	s_mov_b32 m0, s13
	s_barrier
	ds_read_b128 v[204:207], v189 offset:16384
	ds_read_b128 v[216:219], v189 offset:18432
	ds_read_b128 v[208:211], v191 offset:16384
	ds_read_b128 v[220:223], v191 offset:18432
	ds_read_b128 v[224:227], v189 offset:20480
	ds_read_b128 v[232:235], v189 offset:22528
	ds_read_b128 v[228:231], v191 offset:20480
	ds_read_b128 v[236:239], v191 offset:22528
	global_load_lds_dwordx4 v172, s[26:27]
	s_mov_b32 m0, s44
	v_mov_b32_e32 v185, v173
	global_load_lds_dwordx4 v184, s[26:27]
	s_barrier
	s_waitcnt lgkmcnt(0)
	v_lshl_add_u64 v[186:187], s[26:27], 0, v[172:173]
	v_lshl_add_u64 v[184:185], s[26:27], 0, v[184:185]
	s_setprio 1
	s_waitcnt lgkmcnt(0)
	v_mfma_scale_f32_16x16x128_f8f6f4 v[124:127], v[0:7], v[204:211], 0, v188, v188 op_sel_hi:[0,0,0]
	v_mfma_scale_f32_16x16x128_f8f6f4 v[120:123], v[8:15], v[204:211], 0, v188, v188 op_sel_hi:[0,0,0]
	v_mfma_scale_f32_16x16x128_f8f6f4 v[116:119], v[0:7], v[216:223], 0, v188, v188 op_sel_hi:[0,0,0]
	v_mfma_scale_f32_16x16x128_f8f6f4 v[112:115], v[8:15], v[216:223], 0, v188, v188 op_sel_hi:[0,0,0]
	v_mfma_scale_f32_16x16x128_f8f6f4 v[108:111], v[0:7], v[224:231], 0, v188, v188 op_sel_hi:[0,0,0]
	v_mfma_scale_f32_16x16x128_f8f6f4 v[104:107], v[8:15], v[224:231], 0, v188, v188 op_sel_hi:[0,0,0]
	v_mfma_scale_f32_16x16x128_f8f6f4 v[92:95], v[0:7], v[232:239], 0, v188, v188 op_sel_hi:[0,0,0]
	v_mfma_scale_f32_16x16x128_f8f6f4 v[88:91], v[8:15], v[232:239], 0, v188, v188 op_sel_hi:[0,0,0]
	s_setprio 0
	s_barrier
	s_add_u32 s90, s24, 0x20000
	s_addc_u32 s91, s25, 0
	s_mov_b32 m0, s46
	v_lshl_add_u64 v[0:1], s[90:91], 0, v[162:163]
	global_load_lds_dwordx4 v[0:1], off
	s_mov_b32 m0, s47
	v_lshl_add_u64 v[0:1], s[90:91], 0, v[164:165]
	global_load_lds_dwordx4 v[0:1], off
	s_waitcnt vmcnt(6)
	s_barrier
	s_setprio 1
	v_mfma_scale_f32_16x16x128_f8f6f4 v[60:63], v[16:23], v[204:211], 0, v188, v188 op_sel_hi:[0,0,0]
	v_mfma_scale_f32_16x16x128_f8f6f4 v[56:59], v[24:31], v[204:211], 0, v188, v188 op_sel_hi:[0,0,0]
	v_mfma_scale_f32_16x16x128_f8f6f4 v[52:55], v[16:23], v[216:223], 0, v188, v188 op_sel_hi:[0,0,0]
	v_mfma_scale_f32_16x16x128_f8f6f4 v[48:51], v[24:31], v[216:223], 0, v188, v188 op_sel_hi:[0,0,0]
	v_mfma_scale_f32_16x16x128_f8f6f4 v[44:47], v[16:23], v[224:231], 0, v188, v188 op_sel_hi:[0,0,0]
	v_mfma_scale_f32_16x16x128_f8f6f4 v[40:43], v[24:31], v[224:231], 0, v188, v188 op_sel_hi:[0,0,0]
	v_mfma_scale_f32_16x16x128_f8f6f4 v[36:39], v[16:23], v[232:239], 0, v188, v188 op_sel_hi:[0,0,0]
	v_mfma_scale_f32_16x16x128_f8f6f4 v[32:35], v[24:31], v[232:239], 0, v188, v188 op_sel_hi:[0,0,0]
	s_setprio 0
	s_barrier
	ds_read_b128 v[0:3], v190 offset:32768
	ds_read_b128 v[8:11], v190 offset:34816
	ds_read_b128 v[4:7], v192 offset:32768
	ds_read_b128 v[12:15], v192 offset:34816
	s_mov_b32 m0, s50
	v_lshl_add_u64 v[178:179], s[26:27], 0, v[178:179]
	ds_read_b128 v[16:19], v189 offset:32768
	ds_read_b128 v[24:27], v189 offset:34816
	ds_read_b128 v[20:23], v191 offset:32768
	ds_read_b128 v[28:31], v191 offset:34816
	ds_read_b128 v[204:207], v189 offset:36864
	ds_read_b128 v[216:219], v189 offset:38912
	ds_read_b128 v[208:211], v191 offset:36864
	ds_read_b128 v[220:223], v191 offset:38912
	global_load_lds_dwordx4 v[178:179], off
	s_mov_b32 m0, s51
	v_lshl_add_u64 v[176:177], s[26:27], 0, v[176:177]
	global_load_lds_dwordx4 v[176:177], off
	s_waitcnt lgkmcnt(8)
	s_barrier
	s_waitcnt lgkmcnt(0)
	s_setprio 1
	v_mfma_scale_f32_16x16x128_f8f6f4 v[156:159], v[0:7], v[16:23], v[156:159], v188, v188 op_sel_hi:[0,0,0]
	v_mfma_scale_f32_16x16x128_f8f6f4 v[152:155], v[8:15], v[16:23], v[152:155], v188, v188 op_sel_hi:[0,0,0]
	v_mfma_scale_f32_16x16x128_f8f6f4 v[148:151], v[0:7], v[24:31], v[148:151], v188, v188 op_sel_hi:[0,0,0]
	v_mfma_scale_f32_16x16x128_f8f6f4 v[144:147], v[8:15], v[24:31], v[144:147], v188, v188 op_sel_hi:[0,0,0]
	v_mfma_scale_f32_16x16x128_f8f6f4 v[140:143], v[0:7], v[204:211], v[140:143], v188, v188 op_sel_hi:[0,0,0]
	v_mfma_scale_f32_16x16x128_f8f6f4 v[136:139], v[8:15], v[204:211], v[136:139], v188, v188 op_sel_hi:[0,0,0]
	v_mfma_scale_f32_16x16x128_f8f6f4 v[132:135], v[0:7], v[216:223], v[132:135], v188, v188 op_sel_hi:[0,0,0]
	v_mfma_scale_f32_16x16x128_f8f6f4 v[128:131], v[8:15], v[216:223], v[128:131], v188, v188 op_sel_hi:[0,0,0]
	s_setprio 0
	s_barrier
	s_mov_b32 m0, s56
	v_lshl_add_u64 v[176:177], v[180:181], 0, s[40:41]
	ds_read_b128 v[224:227], v190 offset:49152
	ds_read_b128 v[232:235], v190 offset:51200
	ds_read_b128 v[228:231], v192 offset:49152
	ds_read_b128 v[236:239], v192 offset:51200
	global_load_lds_dwordx4 v[176:177], off
	s_mov_b32 m0, s57
	v_lshl_add_u64 v[176:177], v[182:183], 0, s[40:41]
	global_load_lds_dwordx4 v[176:177], off
	s_barrier
	s_waitcnt lgkmcnt(0)
	s_setprio 1
	v_mfma_scale_f32_16x16x128_f8f6f4 v[100:103], v[224:231], v[16:23], v[100:103], v188, v188 op_sel_hi:[0,0,0]
	v_mfma_scale_f32_16x16x128_f8f6f4 v[96:99], v[232:239], v[16:23], v[96:99], v188, v188 op_sel_hi:[0,0,0]
	v_mfma_scale_f32_16x16x128_f8f6f4 v[84:87], v[224:231], v[24:31], v[84:87], v188, v188 op_sel_hi:[0,0,0]
	v_mfma_scale_f32_16x16x128_f8f6f4 v[80:83], v[232:239], v[24:31], v[80:83], v188, v188 op_sel_hi:[0,0,0]
	v_mfma_scale_f32_16x16x128_f8f6f4 v[76:79], v[224:231], v[204:211], v[76:79], v188, v188 op_sel_hi:[0,0,0]
	v_mfma_scale_f32_16x16x128_f8f6f4 v[72:75], v[232:239], v[204:211], v[72:75], v188, v188 op_sel_hi:[0,0,0]
	v_mfma_scale_f32_16x16x128_f8f6f4 v[68:71], v[224:231], v[216:223], v[68:71], v188, v188 op_sel_hi:[0,0,0]
	v_mfma_scale_f32_16x16x128_f8f6f4 v[64:67], v[232:239], v[216:223], v[64:67], v188, v188 op_sel_hi:[0,0,0]
	s_setprio 0
	s_mov_b32 m0, s64
	v_lshl_add_u64 v[186:187], v[186:187], 0, s[40:41]
	s_barrier
	ds_read_b128 v[16:19], v189 offset:49152
	ds_read_b128 v[24:27], v189 offset:51200
	ds_read_b128 v[20:23], v191 offset:49152
	ds_read_b128 v[28:31], v191 offset:51200
	ds_read_b128 v[176:179], v189 offset:53248
	ds_read_b128 v[204:207], v189 offset:55296
	ds_read_b128 v[180:183], v191 offset:53248
	ds_read_b128 v[208:211], v191 offset:55296
	global_load_lds_dwordx4 v[186:187], off
	s_mov_b32 m0, s65
	v_lshl_add_u64 v[184:185], v[184:185], 0, s[40:41]
	global_load_lds_dwordx4 v[184:185], off
	s_barrier
	s_waitcnt lgkmcnt(0)
	s_setprio 1
	v_mfma_scale_f32_16x16x128_f8f6f4 v[124:127], v[0:7], v[16:23], v[124:127], v188, v188 op_sel_hi:[0,0,0]
	v_mfma_scale_f32_16x16x128_f8f6f4 v[120:123], v[8:15], v[16:23], v[120:123], v188, v188 op_sel_hi:[0,0,0]
	v_mfma_scale_f32_16x16x128_f8f6f4 v[116:119], v[0:7], v[24:31], v[116:119], v188, v188 op_sel_hi:[0,0,0]
	v_mfma_scale_f32_16x16x128_f8f6f4 v[112:115], v[8:15], v[24:31], v[112:115], v188, v188 op_sel_hi:[0,0,0]
	v_mfma_scale_f32_16x16x128_f8f6f4 v[108:111], v[0:7], v[176:183], v[108:111], v188, v188 op_sel_hi:[0,0,0]
	v_mfma_scale_f32_16x16x128_f8f6f4 v[104:107], v[8:15], v[176:183], v[104:107], v188, v188 op_sel_hi:[0,0,0]
	v_mfma_scale_f32_16x16x128_f8f6f4 v[92:95], v[0:7], v[204:211], v[92:95], v188, v188 op_sel_hi:[0,0,0]
	v_mfma_scale_f32_16x16x128_f8f6f4 v[88:91], v[8:15], v[204:211], v[88:91], v188, v188 op_sel_hi:[0,0,0]
	s_setprio 0
	s_barrier
	s_add_u32 s24, s24, 0x20080
	s_addc_u32 s25, s25, 0
	s_mov_b32 m0, s70
	v_lshl_add_u64 v[0:1], s[24:25], 0, v[162:163]
	global_load_lds_dwordx4 v[0:1], off
	s_mov_b32 m0, s71
	v_lshl_add_u64 v[0:1], s[24:25], 0, v[164:165]
	global_load_lds_dwordx4 v[0:1], off
	s_waitcnt vmcnt(6)
	s_barrier
	s_setprio 1
	v_mfma_scale_f32_16x16x128_f8f6f4 v[60:63], v[224:231], v[16:23], v[60:63], v188, v188 op_sel_hi:[0,0,0]
	v_mfma_scale_f32_16x16x128_f8f6f4 v[56:59], v[232:239], v[16:23], v[56:59], v188, v188 op_sel_hi:[0,0,0]
	v_mfma_scale_f32_16x16x128_f8f6f4 v[52:55], v[224:231], v[24:31], v[52:55], v188, v188 op_sel_hi:[0,0,0]
	v_mfma_scale_f32_16x16x128_f8f6f4 v[48:51], v[232:239], v[24:31], v[48:51], v188, v188 op_sel_hi:[0,0,0]
	v_mfma_scale_f32_16x16x128_f8f6f4 v[44:47], v[224:231], v[176:183], v[44:47], v188, v188 op_sel_hi:[0,0,0]
	v_mfma_scale_f32_16x16x128_f8f6f4 v[40:43], v[232:239], v[176:183], v[40:43], v188, v188 op_sel_hi:[0,0,0]
	v_mfma_scale_f32_16x16x128_f8f6f4 v[36:39], v[224:231], v[204:211], v[36:39], v188, v188 op_sel_hi:[0,0,0]
	v_mfma_scale_f32_16x16x128_f8f6f4 v[32:35], v[232:239], v[204:211], v[32:35], v188, v188 op_sel_hi:[0,0,0]
	s_setprio 0
	s_add_i32 s85, s85, 2
	s_add_u32 s22, s22, 0x100
	s_addc_u32 s23, s23, 0
	s_add_u32 s7, s7, 0x100
	s_addc_u32 s83, s83, 0
	s_cmp_gt_u32 s85, 5
	s_barrier
	s_branch .LBB0_1667
.LBB0_1666:
	ds_read_b128 v[0:3], v190
	ds_read_b128 v[8:11], v190 offset:2048
	ds_read_b128 v[4:7], v192
	ds_read_b128 v[12:15], v192 offset:2048
	s_add_u32 s26, s22, 0x80
	s_addc_u32 s27, s23, 0
	s_and_b64 s[24:25], s[24:25], exec
	s_cselect_b32 s27, s19, s27
	s_cselect_b32 s26, s18, s26
	s_cselect_b32 s25, s17, s83
	s_cselect_b32 s24, s16, s7
	v_lshl_add_u64 v[16:17], s[22:23], 0, v[166:167]
	s_add_i32 m0, s13, 0xc000
	ds_read_b128 v[204:207], v189
	ds_read_b128 v[216:219], v189 offset:2048
	ds_read_b128 v[208:211], v191
	ds_read_b128 v[220:223], v191 offset:2048
	ds_read_b128 v[224:227], v189 offset:4096
	ds_read_b128 v[232:235], v189 offset:6144
	ds_read_b128 v[228:231], v191 offset:4096
	ds_read_b128 v[236:239], v191 offset:6144
	global_load_lds_dwordx4 v[16:17], off
	s_add_i32 m0, s13, 0xe000
	v_lshl_add_u64 v[16:17], s[22:23], 0, v[170:171]
	global_load_lds_dwordx4 v[16:17], off
	s_waitcnt lgkmcnt(8)
	s_barrier
	s_waitcnt lgkmcnt(0)
	s_setprio 1
	v_mfma_scale_f32_16x16x128_f8f6f4 v[156:159], v[0:7], v[204:211], v[156:159], v188, v188 op_sel_hi:[0,0,0]
	v_mfma_scale_f32_16x16x128_f8f6f4 v[152:155], v[8:15], v[204:211], v[152:155], v188, v188 op_sel_hi:[0,0,0]
	v_mfma_scale_f32_16x16x128_f8f6f4 v[148:151], v[0:7], v[216:223], v[148:151], v188, v188 op_sel_hi:[0,0,0]
	v_mfma_scale_f32_16x16x128_f8f6f4 v[144:147], v[8:15], v[216:223], v[144:147], v188, v188 op_sel_hi:[0,0,0]
	v_mfma_scale_f32_16x16x128_f8f6f4 v[140:143], v[0:7], v[224:231], v[140:143], v188, v188 op_sel_hi:[0,0,0]
	v_mfma_scale_f32_16x16x128_f8f6f4 v[136:139], v[8:15], v[224:231], v[136:139], v188, v188 op_sel_hi:[0,0,0]
	v_mfma_scale_f32_16x16x128_f8f6f4 v[132:135], v[0:7], v[232:239], v[132:135], v188, v188 op_sel_hi:[0,0,0]
	v_mfma_scale_f32_16x16x128_f8f6f4 v[128:131], v[8:15], v[232:239], v[128:131], v188, v188 op_sel_hi:[0,0,0]
	s_setprio 0
	s_barrier
	s_mov_b32 m0, s15
	v_lshl_add_u64 v[180:181], s[24:25], 0, v[162:163]
	ds_read_b128 v[16:19], v190 offset:16384
	ds_read_b128 v[24:27], v190 offset:18432
	ds_read_b128 v[20:23], v192 offset:16384
	ds_read_b128 v[28:31], v192 offset:18432
	global_load_lds_dwordx4 v[180:181], off
	s_mov_b32 m0, s31
	v_lshl_add_u64 v[182:183], s[24:25], 0, v[164:165]
	global_load_lds_dwordx4 v[182:183], off
	s_barrier
	s_waitcnt lgkmcnt(0)
	s_setprio 1
	v_mfma_scale_f32_16x16x128_f8f6f4 v[100:103], v[16:23], v[204:211], v[100:103], v188, v188 op_sel_hi:[0,0,0]
	v_mfma_scale_f32_16x16x128_f8f6f4 v[96:99], v[24:31], v[204:211], v[96:99], v188, v188 op_sel_hi:[0,0,0]
	v_mfma_scale_f32_16x16x128_f8f6f4 v[84:87], v[16:23], v[216:223], v[84:87], v188, v188 op_sel_hi:[0,0,0]
	v_mfma_scale_f32_16x16x128_f8f6f4 v[80:83], v[24:31], v[216:223], v[80:83], v188, v188 op_sel_hi:[0,0,0]
	v_mfma_scale_f32_16x16x128_f8f6f4 v[76:79], v[16:23], v[224:231], v[76:79], v188, v188 op_sel_hi:[0,0,0]
	v_mfma_scale_f32_16x16x128_f8f6f4 v[72:75], v[24:31], v[224:231], v[72:75], v188, v188 op_sel_hi:[0,0,0]
	v_mfma_scale_f32_16x16x128_f8f6f4 v[68:71], v[16:23], v[232:239], v[68:71], v188, v188 op_sel_hi:[0,0,0]
	v_mfma_scale_f32_16x16x128_f8f6f4 v[64:67], v[24:31], v[232:239], v[64:67], v188, v188 op_sel_hi:[0,0,0]
	s_setprio 0
	s_mov_b32 m0, s13
	s_barrier
	ds_read_b128 v[204:207], v189 offset:16384
	ds_read_b128 v[216:219], v189 offset:18432
	ds_read_b128 v[208:211], v191 offset:16384
	ds_read_b128 v[220:223], v191 offset:18432
	ds_read_b128 v[224:227], v189 offset:20480
	ds_read_b128 v[232:235], v189 offset:22528
	ds_read_b128 v[228:231], v191 offset:20480
	ds_read_b128 v[236:239], v191 offset:22528
	global_load_lds_dwordx4 v172, s[26:27]
	s_mov_b32 m0, s44
	v_mov_b32_e32 v185, v173
	global_load_lds_dwordx4 v184, s[26:27]
	s_barrier
	s_waitcnt lgkmcnt(0)
	v_lshl_add_u64 v[186:187], s[26:27], 0, v[172:173]
	v_lshl_add_u64 v[184:185], s[26:27], 0, v[184:185]
	s_setprio 1
	s_waitcnt lgkmcnt(0)
	v_mfma_scale_f32_16x16x128_f8f6f4 v[124:127], v[0:7], v[204:211], v[124:127], v188, v188 op_sel_hi:[0,0,0]
	v_mfma_scale_f32_16x16x128_f8f6f4 v[120:123], v[8:15], v[204:211], v[120:123], v188, v188 op_sel_hi:[0,0,0]
	v_mfma_scale_f32_16x16x128_f8f6f4 v[116:119], v[0:7], v[216:223], v[116:119], v188, v188 op_sel_hi:[0,0,0]
	v_mfma_scale_f32_16x16x128_f8f6f4 v[112:115], v[8:15], v[216:223], v[112:115], v188, v188 op_sel_hi:[0,0,0]
	v_mfma_scale_f32_16x16x128_f8f6f4 v[108:111], v[0:7], v[224:231], v[108:111], v188, v188 op_sel_hi:[0,0,0]
	v_mfma_scale_f32_16x16x128_f8f6f4 v[104:107], v[8:15], v[224:231], v[104:107], v188, v188 op_sel_hi:[0,0,0]
	v_mfma_scale_f32_16x16x128_f8f6f4 v[92:95], v[0:7], v[232:239], v[92:95], v188, v188 op_sel_hi:[0,0,0]
	v_mfma_scale_f32_16x16x128_f8f6f4 v[88:91], v[8:15], v[232:239], v[88:91], v188, v188 op_sel_hi:[0,0,0]
	s_setprio 0
	s_barrier
	s_add_u32 s90, s24, 0x20000
	s_addc_u32 s91, s25, 0
	s_mov_b32 m0, s46
	v_lshl_add_u64 v[0:1], s[90:91], 0, v[162:163]
	global_load_lds_dwordx4 v[0:1], off
	s_mov_b32 m0, s47
	v_lshl_add_u64 v[0:1], s[90:91], 0, v[164:165]
	global_load_lds_dwordx4 v[0:1], off
	s_waitcnt vmcnt(6)
	s_barrier
	s_setprio 1
	v_mfma_scale_f32_16x16x128_f8f6f4 v[60:63], v[16:23], v[204:211], v[60:63], v188, v188 op_sel_hi:[0,0,0]
	v_mfma_scale_f32_16x16x128_f8f6f4 v[56:59], v[24:31], v[204:211], v[56:59], v188, v188 op_sel_hi:[0,0,0]
	v_mfma_scale_f32_16x16x128_f8f6f4 v[52:55], v[16:23], v[216:223], v[52:55], v188, v188 op_sel_hi:[0,0,0]
	v_mfma_scale_f32_16x16x128_f8f6f4 v[48:51], v[24:31], v[216:223], v[48:51], v188, v188 op_sel_hi:[0,0,0]
	v_mfma_scale_f32_16x16x128_f8f6f4 v[44:47], v[16:23], v[224:231], v[44:47], v188, v188 op_sel_hi:[0,0,0]
	v_mfma_scale_f32_16x16x128_f8f6f4 v[40:43], v[24:31], v[224:231], v[40:43], v188, v188 op_sel_hi:[0,0,0]
	v_mfma_scale_f32_16x16x128_f8f6f4 v[36:39], v[16:23], v[232:239], v[36:39], v188, v188 op_sel_hi:[0,0,0]
	v_mfma_scale_f32_16x16x128_f8f6f4 v[32:35], v[24:31], v[232:239], v[32:35], v188, v188 op_sel_hi:[0,0,0]
	s_setprio 0
	s_barrier
	ds_read_b128 v[0:3], v190 offset:32768
	ds_read_b128 v[8:11], v190 offset:34816
	ds_read_b128 v[4:7], v192 offset:32768
	ds_read_b128 v[12:15], v192 offset:34816
	s_mov_b32 m0, s50
	v_lshl_add_u64 v[178:179], s[26:27], 0, v[178:179]
	ds_read_b128 v[16:19], v189 offset:32768
	ds_read_b128 v[24:27], v189 offset:34816
	ds_read_b128 v[20:23], v191 offset:32768
	ds_read_b128 v[28:31], v191 offset:34816
	ds_read_b128 v[204:207], v189 offset:36864
	ds_read_b128 v[216:219], v189 offset:38912
	ds_read_b128 v[208:211], v191 offset:36864
	ds_read_b128 v[220:223], v191 offset:38912
	global_load_lds_dwordx4 v[178:179], off
	s_mov_b32 m0, s51
	v_lshl_add_u64 v[176:177], s[26:27], 0, v[176:177]
	global_load_lds_dwordx4 v[176:177], off
	s_waitcnt lgkmcnt(8)
	s_barrier
	s_waitcnt lgkmcnt(0)
	s_setprio 1
	v_mfma_scale_f32_16x16x128_f8f6f4 v[156:159], v[0:7], v[16:23], v[156:159], v188, v188 op_sel_hi:[0,0,0]
	v_mfma_scale_f32_16x16x128_f8f6f4 v[152:155], v[8:15], v[16:23], v[152:155], v188, v188 op_sel_hi:[0,0,0]
	v_mfma_scale_f32_16x16x128_f8f6f4 v[148:151], v[0:7], v[24:31], v[148:151], v188, v188 op_sel_hi:[0,0,0]
	v_mfma_scale_f32_16x16x128_f8f6f4 v[144:147], v[8:15], v[24:31], v[144:147], v188, v188 op_sel_hi:[0,0,0]
	v_mfma_scale_f32_16x16x128_f8f6f4 v[140:143], v[0:7], v[204:211], v[140:143], v188, v188 op_sel_hi:[0,0,0]
	v_mfma_scale_f32_16x16x128_f8f6f4 v[136:139], v[8:15], v[204:211], v[136:139], v188, v188 op_sel_hi:[0,0,0]
	v_mfma_scale_f32_16x16x128_f8f6f4 v[132:135], v[0:7], v[216:223], v[132:135], v188, v188 op_sel_hi:[0,0,0]
	v_mfma_scale_f32_16x16x128_f8f6f4 v[128:131], v[8:15], v[216:223], v[128:131], v188, v188 op_sel_hi:[0,0,0]
	s_setprio 0
	s_barrier
	s_mov_b32 m0, s56
	v_lshl_add_u64 v[176:177], v[180:181], 0, s[40:41]
	ds_read_b128 v[224:227], v190 offset:49152
	ds_read_b128 v[232:235], v190 offset:51200
	ds_read_b128 v[228:231], v192 offset:49152
	ds_read_b128 v[236:239], v192 offset:51200
	global_load_lds_dwordx4 v[176:177], off
	s_mov_b32 m0, s57
	v_lshl_add_u64 v[176:177], v[182:183], 0, s[40:41]
	global_load_lds_dwordx4 v[176:177], off
	s_barrier
	s_waitcnt lgkmcnt(0)
	s_setprio 1
	v_mfma_scale_f32_16x16x128_f8f6f4 v[100:103], v[224:231], v[16:23], v[100:103], v188, v188 op_sel_hi:[0,0,0]
	v_mfma_scale_f32_16x16x128_f8f6f4 v[96:99], v[232:239], v[16:23], v[96:99], v188, v188 op_sel_hi:[0,0,0]
	v_mfma_scale_f32_16x16x128_f8f6f4 v[84:87], v[224:231], v[24:31], v[84:87], v188, v188 op_sel_hi:[0,0,0]
	v_mfma_scale_f32_16x16x128_f8f6f4 v[80:83], v[232:239], v[24:31], v[80:83], v188, v188 op_sel_hi:[0,0,0]
	v_mfma_scale_f32_16x16x128_f8f6f4 v[76:79], v[224:231], v[204:211], v[76:79], v188, v188 op_sel_hi:[0,0,0]
	v_mfma_scale_f32_16x16x128_f8f6f4 v[72:75], v[232:239], v[204:211], v[72:75], v188, v188 op_sel_hi:[0,0,0]
	v_mfma_scale_f32_16x16x128_f8f6f4 v[68:71], v[224:231], v[216:223], v[68:71], v188, v188 op_sel_hi:[0,0,0]
	v_mfma_scale_f32_16x16x128_f8f6f4 v[64:67], v[232:239], v[216:223], v[64:67], v188, v188 op_sel_hi:[0,0,0]
	s_setprio 0
	s_mov_b32 m0, s64
	v_lshl_add_u64 v[186:187], v[186:187], 0, s[40:41]
	s_barrier
	ds_read_b128 v[16:19], v189 offset:49152
	ds_read_b128 v[24:27], v189 offset:51200
	ds_read_b128 v[20:23], v191 offset:49152
	ds_read_b128 v[28:31], v191 offset:51200
	ds_read_b128 v[176:179], v189 offset:53248
	ds_read_b128 v[204:207], v189 offset:55296
	ds_read_b128 v[180:183], v191 offset:53248
	ds_read_b128 v[208:211], v191 offset:55296
	global_load_lds_dwordx4 v[186:187], off
	s_mov_b32 m0, s65
	v_lshl_add_u64 v[184:185], v[184:185], 0, s[40:41]
	global_load_lds_dwordx4 v[184:185], off
	s_barrier
	s_waitcnt lgkmcnt(0)
	s_setprio 1
	v_mfma_scale_f32_16x16x128_f8f6f4 v[124:127], v[0:7], v[16:23], v[124:127], v188, v188 op_sel_hi:[0,0,0]
	v_mfma_scale_f32_16x16x128_f8f6f4 v[120:123], v[8:15], v[16:23], v[120:123], v188, v188 op_sel_hi:[0,0,0]
	v_mfma_scale_f32_16x16x128_f8f6f4 v[116:119], v[0:7], v[24:31], v[116:119], v188, v188 op_sel_hi:[0,0,0]
	v_mfma_scale_f32_16x16x128_f8f6f4 v[112:115], v[8:15], v[24:31], v[112:115], v188, v188 op_sel_hi:[0,0,0]
	v_mfma_scale_f32_16x16x128_f8f6f4 v[108:111], v[0:7], v[176:183], v[108:111], v188, v188 op_sel_hi:[0,0,0]
	v_mfma_scale_f32_16x16x128_f8f6f4 v[104:107], v[8:15], v[176:183], v[104:107], v188, v188 op_sel_hi:[0,0,0]
	v_mfma_scale_f32_16x16x128_f8f6f4 v[92:95], v[0:7], v[204:211], v[92:95], v188, v188 op_sel_hi:[0,0,0]
	v_mfma_scale_f32_16x16x128_f8f6f4 v[88:91], v[8:15], v[204:211], v[88:91], v188, v188 op_sel_hi:[0,0,0]
	s_setprio 0
	s_barrier
	s_add_u32 s24, s24, 0x20080
	s_addc_u32 s25, s25, 0
	s_mov_b32 m0, s70
	v_lshl_add_u64 v[0:1], s[24:25], 0, v[162:163]
	global_load_lds_dwordx4 v[0:1], off
	s_mov_b32 m0, s71
	v_lshl_add_u64 v[0:1], s[24:25], 0, v[164:165]
	global_load_lds_dwordx4 v[0:1], off
	s_waitcnt vmcnt(6)
	s_barrier
	s_setprio 1
	v_mfma_scale_f32_16x16x128_f8f6f4 v[60:63], v[224:231], v[16:23], v[60:63], v188, v188 op_sel_hi:[0,0,0]
	v_mfma_scale_f32_16x16x128_f8f6f4 v[56:59], v[232:239], v[16:23], v[56:59], v188, v188 op_sel_hi:[0,0,0]
	v_mfma_scale_f32_16x16x128_f8f6f4 v[52:55], v[224:231], v[24:31], v[52:55], v188, v188 op_sel_hi:[0,0,0]
	v_mfma_scale_f32_16x16x128_f8f6f4 v[48:51], v[232:239], v[24:31], v[48:51], v188, v188 op_sel_hi:[0,0,0]
	v_mfma_scale_f32_16x16x128_f8f6f4 v[44:47], v[224:231], v[176:183], v[44:47], v188, v188 op_sel_hi:[0,0,0]
	v_mfma_scale_f32_16x16x128_f8f6f4 v[40:43], v[232:239], v[176:183], v[40:43], v188, v188 op_sel_hi:[0,0,0]
	v_mfma_scale_f32_16x16x128_f8f6f4 v[36:39], v[224:231], v[204:211], v[36:39], v188, v188 op_sel_hi:[0,0,0]
	v_mfma_scale_f32_16x16x128_f8f6f4 v[32:35], v[232:239], v[204:211], v[32:35], v188, v188 op_sel_hi:[0,0,0]
	s_setprio 0
	s_add_i32 s85, s85, 2
	s_add_u32 s22, s22, 0x100
	s_addc_u32 s23, s23, 0
	s_add_u32 s7, s7, 0x100
	s_addc_u32 s83, s83, 0
	s_cmp_gt_u32 s85, 5
	s_barrier
	s_cbranch_scc1 .LBB0_1655
